# v12 config with FFT phase at 56 steps and an extra piggyback site in the layer-0 down GEMM
# baseline (speedup 1.0000x reference)
; __device__ __forceinline__ int tid_fresh() { int t = threadIdx.x; asm volatile("" : "+v"(t)); return t; }
; __device__ __forceinline__ unsigned cvt_pk_bf16(float lo, float hi) { unsigned r; asm volatile("v_cvt_pk_bf16_f32 %0, %1, %2" : "=v"(r) : "v"(lo), "v"(hi)); return r; }
; __device__ __forceinline__ bool bg_decode(int st, int wg, int NW, int lane, KP kp, const float*& src, int& ldS, bf16_t*& dst, int& o2) {
;     const int g = st * NW + wg;
;     if (g >= BG_STEPS) { src = kp->in[27] + lane; ldS = 0; dst = nullptr; o2 = 0; return false; }
; __device__ __forceinline__ void hy_fft_phase(LAS unsigned char* lds, int bid, int G, const bf16_t* vgT, bf16_t* zT, const float* a3, const float* wout, const float* skip, float* filt, float4* gspec) {
;     ...
;             const int tid = tid_fresh(), lane = tid & 63, wave = tid >> 6, col = lane & 15, kc = lane >> 4;
;             const int ci = g0 + (col >> 1), c = bid + G * ci; const bool cok = ci < nch;
;             bf16x8 bw[2];
; #pragma unroll
;             for (int ks = 0; ks < 2; ++ks) { float wv[8];
; #pragma unroll
;                 for (int q = 0; q < 8; ++q) wv[q] = wout[(size_t)(ks * 32 + kc * 8 + q) * 4096 + (col & 1) * D + (cok ? c : bid)] * (cok ? 1.f : 0.f);
;                 u32x4 w; w.x = cvt_pk_bf16(wv[0], wv[1]); w.y = cvt_pk_bf16(wv[2], wv[3]); w.z = cvt_pk_bf16(wv[4], wv[5]); w.w = cvt_pk_bf16(wv[6], wv[7]);
;                 bw[ks] = __builtin_bit_cast(bf16x8, w); }
.LBB0_377:
	v_mov_b32_e32 v14, v0
	v_readlane_b32 s0, v254, 4
	v_bfe_u32 v2, v14, 1, 3
	v_or_b32_e32 v2, s84, v2
	v_mul_lo_u32 v3, v2, s0
	v_readlane_b32 s0, v254, 19
	v_cmp_gt_i32_e32 vcc, s61, v2
	v_lshlrev_b32_e32 v4, 13, v14
	v_add_u32_e32 v16, s0, v3
	v_cndmask_b32_e32 v2, v63, v16, vcc
	v_and_b32_e32 v60, 0x2000, v4
	v_bfe_u32 v15, v14, 4, 2
	v_ashrrev_i32_e32 v3, 31, v2
	v_lshl_add_u64 v[4:5], s[4:5], 0, v[60:61]
	v_lshl_add_u64 v[2:3], v[2:3], 2, v[4:5]
	v_lshlrev_b32_e32 v60, 17, v15
	v_readlane_b32 s1, v254, 20
	v_lshl_add_u64 v[6:7], v[2:3], 0, v[60:61]
	s_movk_i32 s0, 0x4000
	v_add_co_u32_e64 v2, s[0:1], s0, v6
	v_cndmask_b32_e64 v29, 0, 1.0, vcc
	s_nop 0
	v_addc_co_u32_e64 v3, s[0:1], 0, v7, s[0:1]
	s_mov_b32 s0, 0x8000
	s_nop 0
	v_add_co_u32_e64 v4, s[0:1], s0, v6
	s_mul_i32 s28, s60, s16
	s_nop 0
	v_addc_co_u32_e64 v5, s[0:1], 0, v7, s[0:1]
	s_mov_b32 s0, 0xc000
	s_nop 0
	v_add_co_u32_e64 v8, s[0:1], s0, v6
	s_add_i32 s28, s28, s17
	s_nop 0
	v_addc_co_u32_e64 v9, s[0:1], 0, v7, s[0:1]
	v_add_co_u32_e64 v10, s[0:1], s71, v6
	s_cmp_gt_i32 s28, 0x1bfff
	s_nop 0
	v_addc_co_u32_e64 v11, s[0:1], 0, v7, s[0:1]
	v_add_co_u32_e64 v12, s[0:1], s72, v6
	s_mov_b64 s[8:9], -1
	s_nop 0
	v_addc_co_u32_e64 v13, s[0:1], 0, v7, s[0:1]
	v_add_co_u32_e64 v18, s[0:1], s73, v6
	s_nop 1
	v_addc_co_u32_e64 v19, s[0:1], 0, v7, s[0:1]
	v_add_co_u32_e64 v20, s[0:1], s74, v6
	s_nop 1
	v_addc_co_u32_e64 v21, s[0:1], 0, v7, s[0:1]
	global_load_dword v17, v[6:7], off nt
	s_nop 0
	global_load_dword v2, v[2:3], off nt
	s_nop 0
	global_load_dword v3, v[4:5], off nt
	s_nop 0
	global_load_dword v4, v[8:9], off nt
	global_load_dword v5, v[10:11], off nt
	global_load_dword v26, v[12:13], off nt
	global_load_dword v27, v[18:19], off nt
	global_load_dword v28, v[20:21], off nt
	s_mov_b32 s0, 0x80000
	v_add_co_u32_e32 v8, vcc, s0, v6
	s_mov_b32 s0, 0x84000
	s_nop 0
	v_addc_co_u32_e32 v9, vcc, 0, v7, vcc
	v_add_co_u32_e32 v10, vcc, s0, v6
	s_mov_b32 s0, 0x88000
	s_nop 0
	v_addc_co_u32_e32 v11, vcc, 0, v7, vcc
	v_add_co_u32_e32 v12, vcc, s0, v6
	s_mov_b32 s0, 0x8c000
	s_nop 0
	v_addc_co_u32_e32 v13, vcc, 0, v7, vcc
	v_add_co_u32_e32 v18, vcc, s0, v6
	s_mov_b32 s0, 0x90000
	s_nop 0
	v_addc_co_u32_e32 v19, vcc, 0, v7, vcc
	v_add_co_u32_e32 v20, vcc, s0, v6
	s_mov_b32 s0, 0x94000
	s_nop 0
	v_addc_co_u32_e32 v21, vcc, 0, v7, vcc
	v_add_co_u32_e32 v22, vcc, s0, v6
	s_mov_b32 s0, 0x98000
	s_nop 0
	v_addc_co_u32_e32 v23, vcc, 0, v7, vcc
	v_add_co_u32_e32 v24, vcc, s0, v6
	s_mov_b32 s0, 0x9c000
	s_nop 0
	v_addc_co_u32_e32 v25, vcc, 0, v7, vcc
	v_add_co_u32_e32 v6, vcc, s0, v6
	v_readlane_b32 s0, v254, 0
	s_nop 0
	v_addc_co_u32_e32 v7, vcc, 0, v7, vcc
	v_readlane_b32 s1, v254, 1
	s_waitcnt vmcnt(7)
	v_mul_f32_e32 v17, v17, v29
	s_waitcnt vmcnt(6)
	v_mul_f32_e32 v2, v2, v29
	s_waitcnt vmcnt(5)
	v_mul_f32_e32 v3, v3, v29
	s_waitcnt vmcnt(4)
	v_mul_f32_e32 v4, v4, v29
	s_waitcnt vmcnt(3)
	v_mul_f32_e32 v5, v29, v5
	s_waitcnt vmcnt(2)
	v_mul_f32_e32 v26, v29, v26
	s_waitcnt vmcnt(1)
	v_mul_f32_e32 v27, v29, v27
	s_waitcnt vmcnt(0)
	v_mul_f32_e32 v28, v29, v28
	v_cvt_pk_bf16_f32 v2, v17, v2
	v_cvt_pk_bf16_f32 v3, v3, v4
	v_cvt_pk_bf16_f32 v4, v5, v26
	v_cvt_pk_bf16_f32 v5, v27, v28
	global_load_dword v8, v[8:9], off nt
	s_nop 0
	global_load_dword v9, v[10:11], off nt
	s_nop 0
	global_load_dword v10, v[12:13], off nt
	global_load_dword v11, v[18:19], off nt
	s_nop 0
	global_load_dword v12, v[20:21], off nt
	global_load_dword v13, v[22:23], off nt
	global_load_dword v17, v[24:25], off nt
	s_nop 0
	global_load_dword v6, v[6:7], off nt
	s_waitcnt vmcnt(7)
	v_mul_f32_e32 v7, v29, v8
	s_waitcnt vmcnt(6)
	v_mul_f32_e32 v8, v29, v9
	s_waitcnt vmcnt(5)
	v_mul_f32_e32 v9, v29, v10
	s_waitcnt vmcnt(4)
	v_mul_f32_e32 v10, v29, v11
	s_waitcnt vmcnt(3)
	v_mul_f32_e32 v11, v29, v12
	s_waitcnt vmcnt(2)
	v_mul_f32_e32 v12, v29, v13
	s_waitcnt vmcnt(1)
	v_mul_f32_e32 v13, v29, v17
	s_waitcnt vmcnt(0)
	v_mul_f32_e32 v17, v29, v6
	v_cvt_pk_bf16_f32 v6, v7, v8
	v_cvt_pk_bf16_f32 v7, v9, v10
	v_cvt_pk_bf16_f32 v8, v11, v12
	v_cvt_pk_bf16_f32 v9, v13, v17
	s_barrier
	s_cbranch_scc0 .LBB0_379
	s_load_dwordx2 s[8:9], s[0:1], 0xd8
	v_mov_b32_e32 v65, v61
	s_waitcnt lgkmcnt(0)
	v_lshl_add_u64 v[10:11], s[8:9], 0, v[64:65]
	s_mov_b64 s[8:9], 0

; __device__ __forceinline__ bool bg_decode(int st, int wg, int NW, int lane, KP kp, const float*& src, int& ldS, bf16_t*& dst, int& o2) {
;     const int g = st * NW + wg;
;     if (g >= BG_STEPS) { src = kp->in[27] + lane; ldS = 0; dst = nullptr; o2 = 0; return false; }
.LBB0_389:
	v_readlane_b32 s0, v254, 0
	s_add_i32 s33, s28, s53
	v_readlane_b32 s1, v254, 1
	s_cmp_lt_i32 s33, 0x1c000
	s_mov_b64 s[42:43], -1
	s_cbranch_scc1 .LBB0_391
	s_load_dwordx2 s[42:43], s[0:1], 0xd8
	v_mov_b32_e32 v65, v61
	s_waitcnt lgkmcnt(0)
	v_lshl_add_u64 v[10:11], s[42:43], 0, v[64:65]
	s_mov_b64 s[42:43], 0

; __device__ __forceinline__ bool bg_decode(int st, int wg, int NW, int lane, KP kp, const float*& src, int& ldS, bf16_t*& dst, int& o2) {
;     const int g = st * NW + wg;
;     if (g >= BG_STEPS) { src = kp->in[27] + lane; ldS = 0; dst = nullptr; o2 = 0; return false; }
.LBB0_465:
	s_or_b64 exec, exec, s[42:43]
	v_readlane_b32 s42, v254, 0
	s_add_i32 s1, s49, s53
	v_readlane_b32 s43, v254, 1
	s_cmp_lt_i32 s1, 0x1c000
	s_mov_b64 s[44:45], -1
	s_cbranch_scc1 .LBB0_467
	s_load_dwordx2 s[44:45], s[42:43], 0xd8
	v_mov_b32_e32 v65, v61
	s_waitcnt lgkmcnt(0)
	v_lshl_add_u64 v[10:11], s[44:45], 0, v[64:65]
	s_mov_b64 s[44:45], 0

; #define SEG_LD32(dst, off, base) asm volatile("global_load_dword %0, %1, %2" : "=v"(dst) : "v"(off), "s"(base) : "memory")
; #define BG_I(x) bg_issue1<x>(bg, bgwg, bgNW, bglane)
; __device__ __forceinline__ bool bg_decode(int st, int wg, int NW, int lane, KP kp, const float*& src, int& ldS, bf16_t*& dst, int& o2) {
;     const int g = st * NW + wg;
;     if (g >= BG_STEPS) { src = kp->in[27] + lane; ldS = 0; dst = nullptr; o2 = 0; return false; }
; __device__ __forceinline__ void hy_fft_phase(LAS unsigned char* lds, int bid, int G, const bf16_t* vgT, bf16_t* zT, const float* a3, const float* wout, const float* skip, float* filt, float4* gspec) {
;     ...
;             {   unsigned pa[16], pb[16]; float sk[2];
;                 const float* skp = skip; asm volatile("" : "+s"(skp));
; #pragma unroll
;                 for (int i = 0; i < 16; ++i) { const unsigned off = 4u * tid + 2048u * i; SEG_LD32(pa[i], off, A1); SEG_LD32(pb[i], off, A2); }
;                 { const unsigned o1 = 4u * c1, o2 = 4u * c2; SEG_LD32(sk[0], o1, skp); SEG_LD32(sk[1], o2, skp); }
;                 BG_I(1);
.LBB0_543:
	s_or_b32 s0, s87, 1
	v_readlane_b32 s1, v254, 4
	s_cmp_lt_i32 s0, s61
	s_mul_i32 s0, s87, s1
	v_readlane_b32 s42, v254, 19
	s_cselect_b64 s[8:9], -1, 0
	s_add_i32 s0, s0, s42
	v_readlane_b32 s43, v254, 20
	s_add_i32 s1, s0, s1
	s_and_b64 s[42:43], s[8:9], exec
	s_cselect_b32 s28, 0x8000, 0
	s_cselect_b32 s46, s1, s0
	s_sub_i32 s12, s87, s84
	s_lshl_b64 s[42:43], s[12:13], 15
	s_add_u32 s42, s10, s42
	s_addc_u32 s43, s11, s43
	v_mov_b32_e32 v80, v0
	s_mov_b64 s[50:51], s[6:7]
	s_add_u32 s48, s42, s28
	s_barrier
	s_addc_u32 s49, s43, 0
	v_lshlrev_b32_e32 v2, 2, v80
	global_load_dword v81, v2, s[42:43]
	global_load_dword v82, v2, s[48:49]
	v_add_u32_e32 v3, 0x800, v2
	global_load_dword v78, v3, s[42:43]
	global_load_dword v79, v3, s[48:49]
	v_add_u32_e32 v3, 0x1000, v2
	global_load_dword v76, v3, s[42:43]
	global_load_dword v77, v3, s[48:49]
	v_add_u32_e32 v3, 0x1800, v2
	global_load_dword v74, v3, s[42:43]
	global_load_dword v75, v3, s[48:49]
	v_add_u32_e32 v3, 0x2000, v2
	global_load_dword v72, v3, s[42:43]
	global_load_dword v73, v3, s[48:49]
	v_add_u32_e32 v3, 0x2800, v2
	global_load_dword v70, v3, s[42:43]
	global_load_dword v71, v3, s[48:49]
	v_add_u32_e32 v3, 0x3000, v2
	global_load_dword v56, v3, s[42:43]
	global_load_dword v57, v3, s[48:49]
	v_add_u32_e32 v3, 0x3800, v2
	global_load_dword v54, v3, s[42:43]
	global_load_dword v55, v3, s[48:49]
	v_add_u32_e32 v3, 0x4000, v2
	global_load_dword v52, v3, s[42:43]
	global_load_dword v53, v3, s[48:49]
	v_add_u32_e32 v3, 0x4800, v2
	global_load_dword v50, v3, s[42:43]
	global_load_dword v51, v3, s[48:49]
	v_add_u32_e32 v3, 0x5000, v2
	global_load_dword v48, v3, s[42:43]
	global_load_dword v49, v3, s[48:49]
	v_add_u32_e32 v3, 0x5800, v2
	global_load_dword v46, v3, s[42:43]
	global_load_dword v47, v3, s[48:49]
	v_add_u32_e32 v3, 0x6000, v2
	global_load_dword v44, v3, s[42:43]
	global_load_dword v45, v3, s[48:49]
	v_add_u32_e32 v3, 0x6800, v2
	global_load_dword v42, v3, s[42:43]
	global_load_dword v43, v3, s[48:49]
	v_add_u32_e32 v3, 0x7000, v2
	global_load_dword v34, v3, s[42:43]
	global_load_dword v35, v3, s[48:49]
	v_add_u32_e32 v2, 0x7800, v2
	global_load_dword v6, v2, s[42:43]
	s_lshl_b32 s1, s0, 2
	global_load_dword v7, v2, s[48:49]
	s_lshl_b32 s12, s46, 2
	v_mov_b32_e32 v2, s1
	global_load_dword v83, v2, s[50:51]
	v_mov_b32_e32 v2, s12
	global_load_dword v84, v2, s[50:51]
	s_mul_i32 s1, s60, s16
	v_readlane_b32 s42, v254, 0
	s_add_i32 s1, s1, s17
	v_readlane_b32 s43, v254, 1
	s_cmp_lt_i32 s1, 0x1c000
	s_mov_b64 s[48:49], -1
	s_cbranch_scc1 .LBB0_545
	s_load_dwordx2 s[48:49], s[42:43], 0xd8
	v_mov_b32_e32 v65, v61
	s_waitcnt lgkmcnt(0)
	v_lshl_add_u64 v[4:5], s[48:49], 0, v[64:65]
	s_mov_b64 s[48:49], 0

; __device__ __forceinline__ bool bg_decode(int st, int wg, int NW, int lane, KP kp, const float*& src, int& ldS, bf16_t*& dst, int& o2) {
;     const int g = st * NW + wg;
;     if (g >= BG_STEPS) { src = kp->in[27] + lane; ldS = 0; dst = nullptr; o2 = 0; return false; }
.LBB0_555:
	s_or_b64 exec, exec, s[42:43]
	s_add_i32 s1, s60, 1
	s_mul_i32 s1, s1, s16
	v_readlane_b32 s42, v254, 0
	s_add_i32 s1, s1, s17
	v_mov_b32_e32 v57, v0
	v_readlane_b32 s43, v254, 1
	s_cmp_lt_i32 s1, 0x1c000
	s_mov_b64 s[44:45], -1
	s_waitcnt lgkmcnt(0)
	s_barrier
	s_cbranch_scc1 .LBB0_557
	s_load_dwordx2 s[44:45], s[42:43], 0xd8
	v_mov_b32_e32 v65, v61
	s_waitcnt lgkmcnt(0)
	v_lshl_add_u64 v[4:5], s[44:45], 0, v[64:65]
	s_mov_b64 s[44:45], 0

; __device__ __forceinline__ bool bg_decode(int st, int wg, int NW, int lane, KP kp, const float*& src, int& ldS, bf16_t*& dst, int& o2) {
;     const int g = st * NW + wg;
;     if (g >= BG_STEPS) { src = kp->in[27] + lane; ldS = 0; dst = nullptr; o2 = 0; return false; }
.LBB0_569:
	s_or_b64 exec, exec, s[44:45]
	s_add_i32 s1, s60, 2
	s_mul_i32 s1, s1, s16
	v_readlane_b32 s44, v254, 0
	s_add_i32 s1, s1, s17
	v_readlane_b32 s45, v254, 1
	s_cmp_lt_i32 s1, 0x1c000
	s_mov_b64 s[48:49], -1
	s_cbranch_scc1 .LBB0_571
	s_load_dwordx2 s[48:49], s[44:45], 0xd8
	v_mov_b32_e32 v65, v61
	s_waitcnt lgkmcnt(0)
	v_lshl_add_u64 v[2:3], s[48:49], 0, v[64:65]
	s_mov_b64 s[48:49], 0

; __device__ __forceinline__ bool bg_decode(int st, int wg, int NW, int lane, KP kp, const float*& src, int& ldS, bf16_t*& dst, int& o2) {
;     const int g = st * NW + wg;
;     if (g >= BG_STEPS) { src = kp->in[27] + lane; ldS = 0; dst = nullptr; o2 = 0; return false; }
.LBB0_581:
	s_or_b64 exec, exec, s[48:49]
	s_add_i32 s1, s60, 3
	s_mul_i32 s1, s1, s16
	v_readlane_b32 s42, v254, 0
	s_add_i32 s1, s1, s17
	v_readlane_b32 s43, v254, 1
	s_cmp_lt_i32 s1, 0x1c000
	s_mov_b64 s[48:49], -1
	s_cbranch_scc1 .LBB0_583
	s_load_dwordx2 s[48:49], s[42:43], 0xd8
	v_mov_b32_e32 v65, v61
	s_waitcnt lgkmcnt(0)
	v_lshl_add_u64 v[2:3], s[48:49], 0, v[64:65]
	s_mov_b64 s[48:49], 0

; __device__ __forceinline__ bool bg_decode(int st, int wg, int NW, int lane, KP kp, const float*& src, int& ldS, bf16_t*& dst, int& o2) {
;     const int g = st * NW + wg;
;     if (g >= BG_STEPS) { src = kp->in[27] + lane; ldS = 0; dst = nullptr; o2 = 0; return false; }
.LBB0_593:
	s_or_b64 exec, exec, s[48:49]
	s_add_i32 s1, s60, 4
	s_mul_i32 s1, s1, s16
	v_readlane_b32 s44, v254, 0
	s_add_i32 s1, s1, s17
	v_readlane_b32 s45, v254, 1
	s_cmp_lt_i32 s1, 0x1c000
	s_mov_b64 s[48:49], -1
	s_cbranch_scc1 .LBB0_595
	s_load_dwordx2 s[48:49], s[44:45], 0xd8
	v_mov_b32_e32 v65, v61
	s_waitcnt lgkmcnt(0)
	v_lshl_add_u64 v[4:5], s[48:49], 0, v[64:65]
	s_mov_b64 s[48:49], 0

; __device__ __forceinline__ bool bg_decode(int st, int wg, int NW, int lane, KP kp, const float*& src, int& ldS, bf16_t*& dst, int& o2) {
;     const int g = st * NW + wg;
;     if (g >= BG_STEPS) { src = kp->in[27] + lane; ldS = 0; dst = nullptr; o2 = 0; return false; }
.LBB0_608:
	s_or_b64 exec, exec, s[44:45]
	s_add_i32 s1, s60, 5
	s_mul_i32 s1, s1, s16
	v_readlane_b32 s42, v254, 0
	s_add_i32 s1, s1, s17
	v_mov_b32_e32 v6, v0
	v_readlane_b32 s43, v254, 1
	s_cmp_lt_i32 s1, 0x1c000
	s_mov_b64 s[44:45], -1
	s_cbranch_scc1 .LBB0_610
	s_load_dwordx2 s[44:45], s[42:43], 0xd8
	v_mov_b32_e32 v65, v61
	s_waitcnt lgkmcnt(0)
	v_lshl_add_u64 v[8:9], s[44:45], 0, v[64:65]
	s_mov_b64 s[44:45], 0

; #define SEG_LD32(dst, off, base) asm volatile("global_load_dword %0, %1, %2" : "=v"(dst) : "v"(off), "s"(base) : "memory")
; #define BG_I(x) bg_issue1<x>(bg, bgwg, bgNW, bglane)
; __device__ __forceinline__ bool bg_decode(int st, int wg, int NW, int lane, KP kp, const float*& src, int& ldS, bf16_t*& dst, int& o2) {
;     const int g = st * NW + wg;
;     if (g >= BG_STEPS) { src = kp->in[27] + lane; ldS = 0; dst = nullptr; o2 = 0; return false; }
; __device__ __forceinline__ void hy_fft_phase(LAS unsigned char* lds, int bid, int G, const bf16_t* vgT, bf16_t* zT, const float* a3, const float* wout, const float* skip, float* filt, float4* gspec) {
;     ...
;             {   unsigned pa[8], pb[8];
; #pragma unroll
;                 for (int i = 0; i < 8; ++i) { const unsigned off = 4u * tid + 2048u * i; SEG_LD32(pa[i], off, v1); SEG_LD32(pb[i], off, v2); }
;                 BG_I(1);
.LBB0_623:
	s_or_b64 exec, exec, s[42:43]
	s_ashr_i32 s1, s0, 31
	s_add_i32 s12, s60, 6
	s_ashr_i32 s47, s46, 31
	s_lshl_b64 s[42:43], s[0:1], 14
	s_add_u32 s42, s64, s42
	s_addc_u32 s43, s65, s43
	s_lshl_b64 s[48:49], s[46:47], 14
	v_mov_b32_e32 v54, v0
	s_add_u32 s48, s64, s48
	s_barrier
	s_addc_u32 s49, s65, s49
	v_lshlrev_b32_e32 v2, 2, v54
	global_load_dword v55, v2, s[42:43]
	global_load_dword v56, v2, s[48:49]
	v_add_u32_e32 v3, 0x800, v2
	global_load_dword v52, v3, s[42:43]
	global_load_dword v53, v3, s[48:49]
	v_add_u32_e32 v3, 0x1000, v2
	global_load_dword v50, v3, s[42:43]
	global_load_dword v51, v3, s[48:49]
	v_add_u32_e32 v3, 0x1800, v2
	global_load_dword v48, v3, s[42:43]
	global_load_dword v49, v3, s[48:49]
	v_add_u32_e32 v3, 0x2000, v2
	global_load_dword v46, v3, s[42:43]
	global_load_dword v47, v3, s[48:49]
	v_add_u32_e32 v3, 0x2800, v2
	global_load_dword v44, v3, s[42:43]
	global_load_dword v45, v3, s[48:49]
	v_add_u32_e32 v3, 0x3000, v2
	global_load_dword v42, v3, s[42:43]
	global_load_dword v43, v3, s[48:49]
	v_add_u32_e32 v2, 0x3800, v2
	global_load_dword v8, v2, s[42:43]
	global_load_dword v9, v2, s[48:49]
	s_mul_i32 s28, s12, s16
	v_readlane_b32 s42, v254, 0
	s_add_i32 s28, s28, s17
	v_readlane_b32 s43, v254, 1
	s_cmp_gt_i32 s28, 0x1bfff
	s_mov_b64 s[48:49], -1
	s_cbranch_scc0 .LBB0_625
	s_load_dwordx2 s[48:49], s[42:43], 0xd8
	v_mov_b32_e32 v65, v61
	s_waitcnt lgkmcnt(0)
	v_lshl_add_u64 v[6:7], s[48:49], 0, v[64:65]
	s_mov_b64 s[48:49], 0

; __device__ __forceinline__ bool bg_decode(int st, int wg, int NW, int lane, KP kp, const float*& src, int& ldS, bf16_t*& dst, int& o2) {
;     const int g = st * NW + wg;
;     if (g >= BG_STEPS) { src = kp->in[27] + lane; ldS = 0; dst = nullptr; o2 = 0; return false; }
.LBB0_635:
	s_or_b64 exec, exec, s[46:47]
	s_add_i32 s12, s60, 7
	s_mul_i32 s28, s12, s16
	v_readlane_b32 s44, v254, 0
	s_add_i32 s28, s28, s17
	v_mov_b32_e32 v120, v0
	v_readlane_b32 s45, v254, 1
	s_cmp_lt_i32 s28, 0x1c000
	s_mov_b64 s[46:47], -1
	s_waitcnt lgkmcnt(0)
	s_barrier
	s_cbranch_scc1 .LBB0_637
	s_load_dwordx2 s[46:47], s[44:45], 0xd8
	v_mov_b32_e32 v65, v61
	s_waitcnt lgkmcnt(0)
	v_lshl_add_u64 v[4:5], s[46:47], 0, v[64:65]
	s_mov_b64 s[46:47], 0

; __device__ __forceinline__ bool bg_decode(int st, int wg, int NW, int lane, KP kp, const float*& src, int& ldS, bf16_t*& dst, int& o2) {
;     const int g = st * NW + wg;
;     if (g >= BG_STEPS) { src = kp->in[27] + lane; ldS = 0; dst = nullptr; o2 = 0; return false; }
.LBB0_649:
	s_or_b64 exec, exec, s[46:47]
	s_add_i32 s12, s60, 8
	s_mul_i32 s28, s12, s16
	v_readlane_b32 s46, v254, 0
	s_add_i32 s28, s28, s17
	v_readlane_b32 s47, v254, 1
	s_cmp_lt_i32 s28, 0x1c000
	s_mov_b64 s[48:49], -1
	s_cbranch_scc1 .LBB0_651
	s_load_dwordx2 s[48:49], s[46:47], 0xd8
	v_mov_b32_e32 v65, v61
	s_waitcnt lgkmcnt(0)
	v_lshl_add_u64 v[2:3], s[48:49], 0, v[64:65]
	s_mov_b64 s[48:49], 0

; __device__ __forceinline__ bool bg_decode(int st, int wg, int NW, int lane, KP kp, const float*& src, int& ldS, bf16_t*& dst, int& o2) {
;     const int g = st * NW + wg;
;     if (g >= BG_STEPS) { src = kp->in[27] + lane; ldS = 0; dst = nullptr; o2 = 0; return false; }
.LBB0_661:
	s_or_b64 exec, exec, s[48:49]
	s_add_i32 s12, s60, 9
	s_mul_i32 s28, s12, s16
	v_readlane_b32 s44, v254, 0
	s_add_i32 s28, s28, s17
	v_readlane_b32 s45, v254, 1
	s_cmp_lt_i32 s28, 0x1c000
	s_mov_b64 s[48:49], -1
	s_cbranch_scc1 .LBB0_663
	s_load_dwordx2 s[48:49], s[44:45], 0xd8
	v_mov_b32_e32 v65, v61
	s_waitcnt lgkmcnt(0)
	v_lshl_add_u64 v[2:3], s[48:49], 0, v[64:65]
	s_mov_b64 s[48:49], 0

; __device__ __forceinline__ bool bg_decode(int st, int wg, int NW, int lane, KP kp, const float*& src, int& ldS, bf16_t*& dst, int& o2) {
;     const int g = st * NW + wg;
;     if (g >= BG_STEPS) { src = kp->in[27] + lane; ldS = 0; dst = nullptr; o2 = 0; return false; }
.LBB0_673:
	s_or_b64 exec, exec, s[44:45]
	s_add_i32 s12, s60, 10
	s_mul_i32 s28, s12, s16
	v_readlane_b32 s44, v254, 0
	s_add_i32 s28, s28, s17
	v_readlane_b32 s45, v254, 1
	s_cmp_lt_i32 s28, 0x1c000
	s_mov_b64 s[46:47], -1
	s_cbranch_scc1 .LBB0_675
	s_load_dwordx2 s[46:47], s[44:45], 0xd8
	v_mov_b32_e32 v65, v61
	s_waitcnt lgkmcnt(0)
	v_lshl_add_u64 v[4:5], s[46:47], 0, v[64:65]
	s_mov_b64 s[46:47], 0

; #define SEG_LD64(dst, off, base) asm volatile("global_load_dwordx2 %0, %1, %2" : "=v"(dst) : "v"(off), "s"(base) : "memory")
; #define BG_I(x) bg_issue1<x>(bg, bgwg, bgNW, bglane)
; __device__ __forceinline__ bool bg_decode(int st, int wg, int NW, int lane, KP kp, const float*& src, int& ldS, bf16_t*& dst, int& o2) {
;     const int g = st * NW + wg;
;     if (g >= BG_STEPS) { src = kp->in[27] + lane; ldS = 0; dst = nullptr; o2 = 0; return false; }
; __device__ __forceinline__ void hy_fft_phase(LAS unsigned char* lds, int bid, int G, const bf16_t* vgT, bf16_t* zT, const float* a3, const float* wout, const float* skip, float* filt, float4* gspec) {
;     ...
;             {   u32x2 gq[16], gh;
; #pragma unroll
;                 for (int i = 0; i < 16; ++i) { const unsigned off = 8u * tid + 4096u * i; SEG_LD64(gq[i], off, GS); }
;                 { const unsigned off = 8u * (FN / 2); SEG_LD64(gh, off, GS); }
;                 BG_I(0);
.LBB0_688:
	s_or_b64 exec, exec, s[46:47]
	v_mov_b32_e32 v114, v0
	s_add_i32 s12, s60, 11
	v_lshlrev_b32_e32 v4, 3, v114
	global_load_dwordx2 v[38:39], v4, s[20:21]
	v_add_u32_e32 v5, 0x1000, v4
	global_load_dwordx2 v[36:37], v5, s[20:21]
	v_add_u32_e32 v5, 0x2000, v4
	global_load_dwordx2 v[34:35], v5, s[20:21]
	v_add_u32_e32 v5, 0x3000, v4
	global_load_dwordx2 v[32:33], v5, s[20:21]
	v_add_u32_e32 v5, 0x4000, v4
	global_load_dwordx2 v[30:31], v5, s[20:21]
	v_add_u32_e32 v5, 0x5000, v4
	global_load_dwordx2 v[28:29], v5, s[20:21]
	v_add_u32_e32 v5, 0x6000, v4
	global_load_dwordx2 v[26:27], v5, s[20:21]
	v_add_u32_e32 v5, 0x7000, v4
	global_load_dwordx2 v[24:25], v5, s[20:21]
	v_add_u32_e32 v5, 0x8000, v4
	global_load_dwordx2 v[22:23], v5, s[20:21]
	v_add_u32_e32 v5, 0x9000, v4
	global_load_dwordx2 v[20:21], v5, s[20:21]
	v_add_u32_e32 v5, 0xa000, v4
	global_load_dwordx2 v[18:19], v5, s[20:21]
	v_add_u32_e32 v5, 0xb000, v4
	global_load_dwordx2 v[16:17], v5, s[20:21]
	v_add_u32_e32 v5, 0xc000, v4
	global_load_dwordx2 v[14:15], v5, s[20:21]
	v_add_u32_e32 v5, 0xd000, v4
	global_load_dwordx2 v[12:13], v5, s[20:21]
	v_add_u32_e32 v5, 0xe000, v4
	global_load_dwordx2 v[10:11], v5, s[20:21]
	v_add_u32_e32 v4, 0xf000, v4
	global_load_dwordx2 v[8:9], v4, s[20:21]
	global_load_dwordx2 v[6:7], v119, s[20:21]
	s_mul_i32 s28, s12, s16
	v_readlane_b32 s46, v254, 0
	s_add_i32 s28, s28, s17
	v_readlane_b32 s47, v254, 1
	s_cmp_lt_i32 s28, 0x1c000
	s_mov_b64 s[48:49], -1
	s_cbranch_scc1 .LBB0_690
	s_load_dwordx2 s[48:49], s[46:47], 0xd8
	v_mov_b32_e32 v65, v61
	s_waitcnt lgkmcnt(0)
	v_lshl_add_u64 v[40:41], s[48:49], 0, v[64:65]
	s_mov_b64 s[48:49], 0

; __device__ __forceinline__ bool bg_decode(int st, int wg, int NW, int lane, KP kp, const float*& src, int& ldS, bf16_t*& dst, int& o2) {
;     const int g = st * NW + wg;
;     if (g >= BG_STEPS) { src = kp->in[27] + lane; ldS = 0; dst = nullptr; o2 = 0; return false; }
.LBB0_702:
	s_or_b64 exec, exec, s[48:49]
	s_add_i32 s12, s60, 12
	s_mul_i32 s28, s12, s16
	v_readlane_b32 s44, v254, 0
	s_add_i32 s28, s28, s17
	v_mov_b32_e32 v128, v0
	v_readlane_b32 s45, v254, 1
	s_cmp_lt_i32 s28, 0x1c000
	s_mov_b64 s[48:49], -1
	s_waitcnt lgkmcnt(0)
	s_barrier
	s_cbranch_scc1 .LBB0_704
	s_load_dwordx2 s[48:49], s[44:45], 0xd8
	v_mov_b32_e32 v65, v61
	s_waitcnt lgkmcnt(0)
	v_lshl_add_u64 v[2:3], s[48:49], 0, v[64:65]
	s_mov_b64 s[48:49], 0

; __device__ __forceinline__ bool bg_decode(int st, int wg, int NW, int lane, KP kp, const float*& src, int& ldS, bf16_t*& dst, int& o2) {
;     const int g = st * NW + wg;
;     if (g >= BG_STEPS) { src = kp->in[27] + lane; ldS = 0; dst = nullptr; o2 = 0; return false; }
.LBB0_717:
	s_or_b64 exec, exec, s[44:45]
	s_add_i32 s12, s60, 13
	s_mul_i32 s28, s12, s16
	v_readlane_b32 s44, v254, 0
	s_add_i32 s28, s28, s17
	v_readlane_b32 s45, v254, 1
	s_cmp_lt_i32 s28, 0x1c000
	s_mov_b64 s[46:47], -1
	s_cbranch_scc1 .LBB0_719
	s_load_dwordx2 s[46:47], s[44:45], 0xd8
	v_mov_b32_e32 v65, v61
	s_waitcnt lgkmcnt(0)
	v_lshl_add_u64 v[2:3], s[46:47], 0, v[64:65]
	s_mov_b64 s[46:47], 0

; __device__ __forceinline__ bool bg_decode(int st, int wg, int NW, int lane, KP kp, const float*& src, int& ldS, bf16_t*& dst, int& o2) {
;     const int g = st * NW + wg;
;     if (g >= BG_STEPS) { src = kp->in[27] + lane; ldS = 0; dst = nullptr; o2 = 0; return false; }
.LBB0_729:
	s_or_b64 exec, exec, s[46:47]
	s_add_i32 s12, s60, 14
	s_mul_i32 s28, s12, s16
	v_readlane_b32 s46, v254, 0
	s_add_i32 s28, s28, s17
	v_readlane_b32 s47, v254, 1
	s_cmp_lt_i32 s28, 0x1c000
	s_mov_b64 s[48:49], -1
	s_cbranch_scc1 .LBB0_731
	s_load_dwordx2 s[48:49], s[46:47], 0xd8
	v_mov_b32_e32 v65, v61
	s_waitcnt lgkmcnt(0)
	v_lshl_add_u64 v[2:3], s[48:49], 0, v[64:65]
	s_mov_b64 s[48:49], 0

; __device__ __forceinline__ bool bg_decode(int st, int wg, int NW, int lane, KP kp, const float*& src, int& ldS, bf16_t*& dst, int& o2) {
;     const int g = st * NW + wg;
;     if (g >= BG_STEPS) { src = kp->in[27] + lane; ldS = 0; dst = nullptr; o2 = 0; return false; }
.LBB0_741:
	s_or_b64 exec, exec, s[48:49]
	s_add_i32 s12, s60, 15
	s_mul_i32 s28, s12, s16
	v_readlane_b32 s44, v254, 0
	s_add_i32 s28, s28, s17
	v_readlane_b32 s45, v254, 1
	s_cmp_lt_i32 s28, 0x1c000
	s_mov_b64 s[48:49], -1
	s_cbranch_scc1 .LBB0_743
	s_load_dwordx2 s[48:49], s[44:45], 0xd8
	v_mov_b32_e32 v65, v61
	s_waitcnt lgkmcnt(0)
	v_lshl_add_u64 v[2:3], s[48:49], 0, v[64:65]
	s_mov_b64 s[48:49], 0

; #define BG_I(x) bg_issue1<x>(bg, bgwg, bgNW, bglane)
; __device__ __forceinline__ bool bg_decode(int st, int wg, int NW, int lane, KP kp, const float*& src, int& ldS, bf16_t*& dst, int& o2) {
;     const int g = st * NW + wg;
;     if (g >= BG_STEPS) { src = kp->in[27] + lane; ldS = 0; dst = nullptr; o2 = 0; return false; }
; __device__ __forceinline__ void hy_fft_phase(LAS unsigned char* lds, int bid, int G, const bf16_t* vgT, bf16_t* zT, const float* a3, const float* wout, const float* skip, float* filt, float4* gspec) {
;     ...
;     { const int nst = (BG_STEPS + bgNW - 1) / bgNW;
;       if (bg.st < nst) { BG_I(0);
.LBB0_775:
	s_abs_i32 s0, s16
	v_cvt_f32_u32_e32 v1, s0
	s_sub_i32 s3, 0, s0
	s_add_i32 s1, s16, 0x1bfff
	s_xor_b32 s2, s1, s16
	v_rcp_iflag_f32_e32 v1, v1
	s_abs_i32 s1, s1
	s_ashr_i32 s2, s2, 31
	v_mul_f32_e32 v1, 0x4f7ffffe, v1
	v_cvt_u32_f32_e32 v1, v1
	s_nop 0
	v_readfirstlane_b32 s4, v1
	s_mul_i32 s3, s3, s4
	s_mul_hi_u32 s3, s4, s3
	s_add_i32 s4, s4, s3
	s_mul_hi_u32 s3, s1, s4
	s_mul_i32 s4, s3, s0
	s_sub_i32 s1, s1, s4
	s_add_i32 s5, s3, 1
	s_sub_i32 s4, s1, s0
	s_cmp_ge_u32 s1, s0
	s_cselect_b32 s3, s5, s3
	s_cselect_b32 s1, s4, s1
	s_add_i32 s4, s3, 1
	s_cmp_ge_u32 s1, s0
	s_cselect_b32 s0, s4, s3
	s_xor_b32 s0, s0, s2
	s_sub_i32 s12, s0, s2
	s_cmp_lt_i32 s60, s12
	s_cbranch_scc0 .LBB0_816
	s_mul_i32 s6, s60, s16
	v_readlane_b32 s0, v254, 0
	s_add_i32 s6, s6, s17
	v_readlane_b32 s1, v254, 1
	s_cmp_lt_i32 s6, 0x1c000
	s_cbranch_scc1 .LBB0_779
	s_load_dwordx2 s[2:3], s[0:1], 0xd8
	v_lshlrev_b32_e32 v2, 2, v58
	v_mov_b32_e32 v3, 0
	s_waitcnt lgkmcnt(0)
	v_lshl_add_u64 v[4:5], s[2:3], 0, v[2:3]
	s_cbranch_execz .LBB0_780
	s_mov_b64 s[2:3], 0
	v_mov_b64_e32 v[2:3], 0
	s_mov_b32 s0, 0
	s_branch .LBB0_786

; #define BG_I(x) bg_issue1<x>(bg, bgwg, bgNW, bglane)
; #define BG_F(y) bg_finish1<y, 32>(bg)
; __device__ __forceinline__ bool bg_decode(int st, int wg, int NW, int lane, KP kp, const float*& src, int& ldS, bf16_t*& dst, int& o2) {
;     const int g = st * NW + wg;
;     if (g >= BG_STEPS) { src = kp->in[27] + lane; ldS = 0; dst = nullptr; o2 = 0; return false; }
; __device__ __forceinline__ void hy_fft_phase(LAS unsigned char* lds, int bid, int G, const bf16_t* vgT, bf16_t* zT, const float* a3, const float* wout, const float* skip, float* filt, float4* gspec) {
;     ...
;       if (bg.st < nst) { BG_I(0);
; #pragma unroll 1
;         while (bg.st < nst) { BG_I(1); BG_F(0); BG_I(0); BG_F(1); }
;         bg_finish1<0, 0>(bg); } }
.LBB0_789:
	v_readlane_b32 s6, v254, 0
	s_add_i32 s1, s14, s17
	v_readlane_b32 s7, v254, 1
	s_mov_b64 s[8:9], -1
	s_cmp_lt_i32 s1, 0x1c000
	v_lshlrev_b32_e32 v12, 2, v58
	s_cbranch_scc1 .LBB0_791
	s_load_dwordx2 s[8:9], s[6:7], 0xd8
	v_mov_b32_e32 v13, v5
	s_waitcnt lgkmcnt(0)
	v_lshl_add_u64 v[14:15], s[8:9], 0, v[12:13]
	s_mov_b64 s[8:9], 0

; #define BG_I(x) bg_issue1<x>(bg, bgwg, bgNW, bglane)
; #define BG_F(y) bg_finish1<y, 32>(bg)
; __device__ __forceinline__ bool bg_decode(int st, int wg, int NW, int lane, KP kp, const float*& src, int& ldS, bf16_t*& dst, int& o2) {
;     const int g = st * NW + wg;
;     if (g >= BG_STEPS) { src = kp->in[27] + lane; ldS = 0; dst = nullptr; o2 = 0; return false; }
; __device__ __forceinline__ void hy_fft_phase(LAS unsigned char* lds, int bid, int G, const bf16_t* vgT, bf16_t* zT, const float* a3, const float* wout, const float* skip, float* filt, float4* gspec) {
;     ...
;       if (bg.st < nst) { BG_I(0);
; #pragma unroll 1
;         while (bg.st < nst) { BG_I(1); BG_F(0); BG_I(0); BG_F(1); }
;         bg_finish1<0, 0>(bg); } }
.LBB0_801:
	s_or_b64 exec, exec, s[8:9]
	v_readlane_b32 s0, v254, 0
	s_add_i32 s7, s22, s17
	v_readlane_b32 s1, v254, 1
	s_cmp_lt_i32 s7, 0x1c000
	s_mov_b64 s[8:9], -1
	s_cbranch_scc1 .LBB0_803
	s_load_dwordx2 s[8:9], s[0:1], 0xd8
	v_mov_b32_e32 v13, v5
	s_waitcnt lgkmcnt(0)
	v_lshl_add_u64 v[14:15], s[8:9], 0, v[12:13]
	s_mov_b64 s[8:9], 0

; #define PG8_WAIT_V(n) asm volatile("s_waitcnt vmcnt(" #n ")" ::: "memory")
; #define PG8_BAR __builtin_amdgcn_s_barrier()
;     __device__ __forceinline__ const char* a_base() const { return (const char*)A; }
;     __device__ __forceinline__ const char* a_base() const { return (const char*)A; }
; template <class Epi, class Sched>
; __device__ __forceinline__ void gemm_phase(LAS unsigned char* lds, const int K, const Sched& S, const Epi& E) {
;     ...
;     Unit cur, nxt; int ui = 0;
;     if (!S.next(0, cur)) return;
;     f32x4 acc[2][2][4][2];
; #pragma unroll
;     for (int a = 0; a < 2; ++a)
; #pragma unroll
;         for (int b = 0; b < 2; ++b)
; #pragma unroll
;             for (int m = 0; m < 4; ++m)
; #pragma unroll
;                 for (int n = 0; n < 2; ++n) acc[a][b][m][n] = (f32x4){0.f, 0.f, 0.f, 0.f};
;     bf16x8 At[4][2], B0[2][2], B1[2][2];
;     const char* const gA = S.a_base();
;     unsigned c00, c01, c10, c11, n00, n01, n10, n11;
;     PG8_AOFFS(cur, c00, c01, c10, c11);
;     const char* cB = S.b_ptr(cur);
;     PG8_STAGE(PG8_SB(0, 0), cB, voffB0, voffB1); PG8_STAGE(PG8_SA(0, 0), gA, c00, c01); PG8_STAGE(PG8_SB(0, 1), cB + hstep, voffB0, voffB1); PG8_STAGE(PG8_SA(0, 1), gA, c10, c11);
;     if (wr == 1) PG8_BAR;
;     PG8_WAIT_V(4); PG8_BAR;
;     PG8_STAGE(PG8_SB(1, 0), cB + kstepB, voffB0, voffB1); PG8_STAGE(PG8_SA(1, 0), gA + kstep, c00, c01); PG8_STAGE(PG8_SB(1, 1), cB + hstep + kstepB, voffB0, voffB1);
;     PG8_WAIT_V(6); PG8_BAR;
;     __device__ __forceinline__ bool next(int i, Unit& u) const {
;         const int L = i * G + c; if (L >= ntiles * 8) return false;
;         const int rt = L >> 3; u.pn = L & 7; u.e = tile_e[rt]; u.pm = rt - tstart[u.e]; u.rbase = (u.e < NE) ? rt * BM : SLOT_SH + u.pm * BM; return true;
;     }
;     __device__ __forceinline__ const char* a_base() const { return (const char*)A; }
;     __device__ __forceinline__ unsigned a_off(const Unit& u, int r) const { return (unsigned)((u.rbase + r) * FF) * 2u; }
;     __device__ __forceinline__ void a_off4(const Unit& u, int r0, int r1, unsigned& o00, unsigned& o01, unsigned& o10, unsigned& o11) const { o00 = a_off(u, r0); o01 = a_off(u, r1); o10 = a_off(u, HALF + r0); o11 = a_off(u, HALF + r1); }
;     __device__ __forceinline__ const char* b_ptr(const Unit& u) const { return (const char*)(W + (size_t)u.e * D * FF + (size_t)u.pn * BM * 8); }
.LBB0_1152:
	s_or_b64 exec, exec, s[0:1]
	v_readlane_b32 s0, v254, 0
	v_readlane_b32 s2, v254, 5
	v_readlane_b32 s1, v254, 1
	s_lshl_b32 s15, s28, 3
	s_and_b32 s3, s2, 7
	v_mov_b32_e32 v2, v0
	s_waitcnt lgkmcnt(0)
	s_barrier
	v_readlane_b32 s84, v254, 0
	v_readlane_b32 s85, v254, 1
	s_nop 1
	s_load_dwordx2 s[74:75], s[84:85], 0xd8
	s_load_dwordx2 s[76:77], s[84:85], 0xe0
	s_load_dwordx2 s[78:79], s[84:85], 0x118
	v_and_b32_e32 v252, 63, v0
	v_lshrrev_b32_e32 v253, 6, v0
	v_lshlrev_b32_e32 v238, 2, v252
	v_lshlrev_b32_e32 v252, 4, v252
	v_add_u32_e32 v239, 0x800, v238
	v_add_u32_e32 v240, 0x1000, v238
	v_add_u32_e32 v241, 0x1800, v238
	v_readlane_b32 s86, v254, 4
	v_readlane_b32 s87, v255, 40
	v_readfirstlane_b32 s88, v253
	s_nop 3
	s_lshl_b32 s71, s86, 3
	s_lshl_b32 s87, s87, 3
	s_add_u32 s87, s87, s88
	s_add_u32 s70, s87, 0x1c000
	s_mov_b32 s80, 0
	s_mov_b32 s82, 0
	s_mov_b32 s90, 0
	s_waitcnt lgkmcnt(0)
	v_writelane_b32 v254, s3, 39
	s_cmp_lt_i32 s2, s15
	s_nop 0
	v_readfirstlane_b32 s33, v2
	s_cbranch_scc0 .LBB0_1166
	v_ashrrev_i32_e32 v1, 31, v2
	v_lshrrev_b32_e32 v1, 26, v1
	v_add_u32_e32 v1, v2, v1
	v_ashrrev_i32_e32 v4, 6, v1
	v_bfe_i32 v1, v2, 27, 1
	v_lshlrev_b32_e32 v3, 4, v2
	v_lshrrev_b32_e32 v1, 22, v1
	v_add_u32_e32 v1, v3, v1
	v_and_b32_e32 v1, 0xfffffc00, v1
	v_sub_u32_e32 v1, v3, v1
	v_lshrrev_b32_e32 v5, 4, v1
	v_bitop3_b32 v5, v5, v1, 32 bitop3:0x6c
	v_ashrrev_i32_e32 v1, 31, v1
	v_lshrrev_b32_e32 v1, 26, v1
	v_lshlrev_b32_e32 v6, 3, v4
	v_add_u32_e32 v1, v5, v1
	v_and_b32_e32 v6, -16, v6
	v_ashrrev_i32_e32 v7, 6, v1
	v_add_u32_e32 v3, 0x2000, v3
	v_add_u32_e32 v1, v7, v6
	v_ashrrev_i32_e32 v6, 31, v3
	v_lshrrev_b32_e32 v6, 22, v6
	v_add_u32_e32 v6, v3, v6
	s_load_dwordx2 s[0:1], s[0:1], 0x118
	v_ashrrev_i32_e32 v6, 10, v6
	v_mul_i32_i24_e32 v8, 0x400, v6
	v_sub_u32_e32 v3, v3, v8
	v_lshrrev_b32_e32 v8, 4, v3
	v_bitop3_b32 v3, v8, v3, 32 bitop3:0x6c
	s_waitcnt lgkmcnt(0)
	s_add_u32 s2, s0, 0x3ee90000
	v_ashrrev_i32_e32 v9, 31, v3
	s_addc_u32 s3, s1, 0
	v_lshrrev_b32_e32 v9, 26, v9
	s_add_u32 s46, s0, 0x24830000
	v_add_u32_e32 v9, v3, v9
	s_addc_u32 s47, s1, 0
	s_ashr_i32 s11, s33, 6
	v_lshlrev_b32_e32 v8, 3, v6
	v_ashrrev_i32_e32 v10, 6, v9
	v_readlane_b32 s4, v254, 39
	v_and_b32_e32 v9, 0xc0, v9
	s_ashr_i32 s10, s33, 8
	v_and_b32_e32 v8, -16, v8
	s_lshl_b32 s48, s11, 10
	s_lshl_b32 s4, s4, 12
	v_lshlrev_b32_e32 v6, 5, v6
	v_sub_u32_e32 v3, v3, v9
	v_mov_b32_e32 v9, 1
	v_add_u32_e32 v146, v10, v8
	s_add_u32 s8, s46, s4
	v_readlane_b32 s4, v254, 5
	v_and_b32_e32 v6, 32, v6
	v_ashrrev_i16_sdwa v3, v9, sext(v3) dst_sel:DWORD dst_unused:UNUSED_PAD src0_sel:DWORD src1_sel:BYTE_0
	s_addc_u32 s9, s47, 0
	s_ashr_i32 s12, s4, 3
	v_and_b32_e32 v8, 3, v10
	s_mov_b32 s5, 0xfffffe0
	v_lshlrev_b32_e32 v10, 1, v146
	v_lshrrev_b32_e32 v11, 2, v146
	v_add_u32_sdwa v3, v6, sext(v3) dst_sel:DWORD dst_unused:UNUSED_PAD src0_sel:DWORD src1_sel:WORD_0
	s_lshl_b32 s4, s12, 2
	v_and_or_b32 v8, v146, s5, v8
	v_and_b32_e32 v10, 24, v10
	v_and_b32_e32 v11, 4, v11
	v_lshlrev_b32_e32 v6, 8, v3
	s_add_i32 s4, s4, 0
	v_or3_b32 v8, v8, v10, v11
	v_and_b32_e32 v6, 0xffff800, v6
	s_add_i32 s4, s4, 0x21160
	v_add_lshl_u32 v130, v8, v6, 4
	v_and_b32_e32 v6, 3, v7
	v_mul_i32_i24_e32 v7, 64, v7
	v_sub_u32_e32 v5, v5, v7
	v_mov_b32_e32 v7, s4
	ds_read_b32 v7, v7
	v_lshlrev_b32_e32 v8, 1, v1
	v_lshrrev_b32_e32 v10, 2, v1
	v_and_or_b32 v6, v1, s5, v6
	v_and_b32_e32 v8, 24, v8
	v_and_b32_e32 v10, 4, v10
	v_or3_b32 v6, v6, v8, v10
	s_waitcnt lgkmcnt(0)
	v_lshlrev_b32_e32 v8, 2, v7
	v_add_u32_e32 v8, 0, v8
	v_add_u32_e32 v8, 0x21040, v8
	ds_read_b32 v8, v8
	s_lshl_b32 s13, s12, 8
	v_readfirstlane_b32 s4, v7
	s_ashr_i32 s5, s4, 31
	v_lshlrev_b32_e32 v4, 5, v4
	s_waitcnt lgkmcnt(0)
	v_readfirstlane_b32 s14, v8
	s_sub_i32 s12, s12, s14
	s_lshl_b32 s12, s12, 8
	v_cmp_lt_i64_e64 s[6:7], s[4:5], 64
	s_add_i32 s12, s12, 0xff00
	v_and_b32_e32 v4, 32, v4
	v_ashrrev_i16_sdwa v5, v9, sext(v5) dst_sel:DWORD dst_unused:UNUSED_PAD src0_sel:DWORD src1_sel:BYTE_0
	s_and_b64 s[6:7], s[6:7], exec
	v_add_u32_sdwa v4, v4, sext(v5) dst_sel:DWORD dst_unused:UNUSED_PAD src0_sel:DWORD src1_sel:WORD_0
	s_cselect_b32 s12, s13, s12
	s_lshl_b64 s[4:5], s[4:5], 21
	v_lshlrev_b32_e32 v5, 8, v4
	s_add_u32 s38, s8, s4
	v_and_b32_e32 v5, 0xffff800, v5
	s_addc_u32 s39, s9, s5
	s_add_i32 s49, s48, 0
	v_add_lshl_u32 v132, v6, v5, 4
	s_add_i32 m0, s49, 0x10000
	v_add_u32_e32 v5, s12, v1
	v_lshlrev_b32_e32 v149, 1, v4
	v_mov_b32_e32 v135, 0
	global_load_lds_dwordx4 v132, s[38:39]
	s_add_i32 m0, s49, 0x12000
	v_add_u32_e32 v6, s12, v146
	v_add_u32_e32 v147, 0x80, v1
	v_lshl_add_u32 v134, v5, 10, v149
	v_lshlrev_b32_e32 v150, 1, v3
	v_mov_b32_e32 v133, v135
	global_load_lds_dwordx4 v130, s[38:39]
	s_mov_b32 m0, s49
	s_add_i32 s50, s49, 0x2000
	v_add_u32_e32 v7, s12, v147
	v_lshl_add_u32 v136, v6, 10, v150
	v_lshl_add_u64 v[4:5], s[38:39], 0, v[132:133]
	v_mov_b32_e32 v131, v135
	global_load_lds_dwordx4 v134, s[2:3]
	s_mov_b32 m0, s50
	s_mov_b64 s[4:5], 0x800
	v_lshl_add_u32 v138, v7, 10, v149
	v_lshl_add_u64 v[6:7], s[38:39], 0, v[130:131]
	global_load_lds_dwordx4 v136, s[2:3]
	v_lshl_add_u64 v[4:5], v[4:5], 0, s[4:5]
	s_add_i32 m0, s49, 0x14000
	v_add_u32_e32 v148, 0x80, v146
	global_load_lds_dwordx4 v[4:5], off
	v_lshl_add_u64 v[4:5], v[6:7], 0, s[4:5]
	s_add_i32 m0, s49, 0x16000
	s_add_i32 s51, s49, 0x4000
	v_add_u32_e32 v8, s12, v148
	global_load_lds_dwordx4 v[4:5], off
	s_mov_b32 m0, s51
	s_add_i32 s52, s49, 0x6000
	v_lshl_add_u32 v140, v8, 10, v150
	global_load_lds_dwordx4 v138, s[2:3]
	s_mov_b32 m0, s52
	s_mov_b32 s53, 0
	global_load_lds_dwordx4 v140, s[2:3]
	s_mov_b32 s54, 0x10000
	s_cmp_lg_u32 s10, 1
	v_mov_b32_e32 v137, v135
	s_cbranch_scc1 .LBB0_1155
	s_barrier

; __device__ __forceinline__ unsigned cvt_pk_bf16(float lo, float hi) { unsigned r; asm volatile("v_cvt_pk_bf16_f32 %0, %1, %2" : "=v"(r) : "v"(lo), "v"(hi)); return r; }
; #define PG8_STAGE(bufoff, gbase, v0, v1) do { \
;         __builtin_amdgcn_global_load_lds((const unsigned*)((const char*)(gbase) + (v0)), (LAS unsigned*)(lds + (bufoff) + ldsw), 16, 0, 0); \
;         __builtin_amdgcn_global_load_lds((const unsigned*)((const char*)(gbase) + (v1)), (LAS unsigned*)(lds + (bufoff) + ldsw + 8192), 16, 0, 0); } while (0)
; #define PG8_LDA(dst, b, h) do { _Pragma("unroll") for (int m = 0; m < 4; ++m) _Pragma("unroll") for (int k = 0; k < 2; ++k) dst[m][k] = *(const LAS bf16x8*)(lds + PG8_SA(b, h) + aoff + m * 2048 + k * 1024); } while (0)
; #define PG8_WAIT_V(n) asm volatile("s_waitcnt vmcnt(" #n ")" ::: "memory")
; #define PG8_WAIT_L(n) asm volatile("s_waitcnt lgkmcnt(" #n ")" ::: "memory")
; template <class Epi, class Sched>
; __device__ __forceinline__ void gemm_phase(LAS unsigned char* lds, const int K, const Sched& S, const Epi& E) {
;     ...
;             PG8_LDB(B0, 0, 0); PG8_SCHED; PG8_LDA(At, 0, 0); PG8_STAGE(PG8_SA(1, 1), a1, c10, c11);
;             PG8_WAIT_L(8); PG8_BAR; PG8_WAIT_L(0); PG8_MMA(0, 0, At, B0); PG8_BAR; PG8_SCHED;
;             PG8_LDB(B1, 0, 1); PG8_STAGE(PG8_SB(0, 0), b2, voffB0, voffB1);
;             PG8_BAR; PG8_WAIT_L(0); PG8_MMA(0, 1, At, B1); PG8_BAR;
;             PG8_LDA(At, 0, 1); PG8_STAGE(PG8_SA(0, 0), a2, x00, x01);
;             PG8_BAR; PG8_WAIT_L(0); PG8_MMA(1, 0, At, B0); PG8_BAR; PG8_SCHED;
;             PG8_STAGE(PG8_SB(0, 1), b2 + hstep, voffB0, voffB1);
;             PG8_WAIT_V(6); PG8_BAR; PG8_MMA(1, 1, At, B1); PG8_BAR;
; template <int BANK, int WAITN> __device__ __forceinline__ void bg_finish1(BgState& b) {
;     ...
;     if (dst != nullptr) {
; #pragma unroll
;         for (int c = 0; c < 4; ++c) { u32x4 w;
;             w.x = cvt_pk_bf16(b.r[(BANK * 8 + 0) * 4 + c], b.r[(BANK * 8 + 1) * 4 + c]); w.y = cvt_pk_bf16(b.r[(BANK * 8 + 2) * 4 + c], b.r[(BANK * 8 + 3) * 4 + c]);
;             w.z = cvt_pk_bf16(b.r[(BANK * 8 + 4) * 4 + c], b.r[(BANK * 8 + 5) * 4 + c]); w.w = cvt_pk_bf16(b.r[(BANK * 8 + 6) * 4 + c], b.r[(BANK * 8 + 7) * 4 + c]);
;             bf16_t* dp = dst + (c & 1) * 512 + (c >> 1) * b.o2[BANK];
;             asm volatile("global_store_dwordx4 %0, %1, off\n\ts_nop 1" :: "v"(dp), "v"(w) : "memory"); }
.LBB0_1161:
	s_add_u32 s40, s0, s38
	ds_read_b128 v[164:167], v153
	ds_read_b128 v[168:171], v153 offset:1024
	ds_read_b128 v[172:175], v153 offset:2048
	ds_read_b128 v[176:179], v153 offset:3072
	s_addc_u32 s41, s1, s39
	s_add_u32 s42, s40, 0x3ee90100
	s_addc_u32 s43, s41, 0
	s_cmpk_eq_i32 s38, 0x300
	s_cselect_b64 vcc, -1, 0
	s_and_b64 s[40:41], vcc, exec
	v_cndmask_b32_e32 v134, v162, v157, vcc
	s_cselect_b32 s45, s3, s43
	s_cselect_b32 s44, s2, s42
	v_cndmask_b32_e32 v139, v138, v159, vcc
	s_cselect_b32 s41, s37, s31
	s_cselect_b32 s40, s36, s29
	v_cndmask_b32_e32 v204, v136, v158, vcc
	s_add_u32 s42, s40, 0x40000
	s_addc_u32 s43, s41, 0
	v_lshl_add_u64 v[206:207], v[144:145], 0, s[38:39]
	s_add_i32 m0, s49, 0xc000
	ds_read_b128 v[180:183], v154
	ds_read_b128 v[184:187], v154 offset:1024
	ds_read_b128 v[188:191], v154 offset:2048
	ds_read_b128 v[192:195], v154 offset:3072
	ds_read_b128 v[196:199], v154 offset:4096
	ds_read_b128 v[200:203], v154 offset:5120
	ds_read_b128 v[208:211], v154 offset:6144
	ds_read_b128 v[212:215], v154 offset:7168
	global_load_lds_dwordx4 v[206:207], off
	v_lshl_add_u64 v[206:207], v[142:143], 0, s[38:39]
	s_add_i32 m0, s49, 0xe000
	s_nop 0
	global_load_lds_dwordx4 v[206:207], off
	s_waitcnt lgkmcnt(8)
	s_barrier
	s_waitcnt lgkmcnt(0)
	s_setprio 1
	s_waitcnt lgkmcnt(0)
	v_mfma_f32_16x16x32_bf16 v[126:129], v[164:167], v[180:183], v[126:129]
	v_mfma_f32_16x16x32_bf16 v[122:125], v[172:175], v[180:183], v[122:125]
	v_mfma_f32_16x16x32_bf16 v[114:117], v[164:167], v[188:191], v[114:117]
	v_mfma_f32_16x16x32_bf16 v[106:109], v[172:175], v[188:191], v[106:109]
	v_mfma_f32_16x16x32_bf16 v[98:101], v[164:167], v[196:199], v[98:101]
	v_mfma_f32_16x16x32_bf16 v[90:93], v[172:175], v[196:199], v[90:93]
	v_mfma_f32_16x16x32_bf16 v[82:85], v[164:167], v[208:211], v[82:85]
	v_mfma_f32_16x16x32_bf16 v[74:77], v[172:175], v[208:211], v[74:77]
	v_mfma_f32_16x16x32_bf16 v[126:129], v[168:171], v[184:187], v[126:129]
	v_mfma_f32_16x16x32_bf16 v[122:125], v[176:179], v[184:187], v[122:125]
	v_mfma_f32_16x16x32_bf16 v[114:117], v[168:171], v[192:195], v[114:117]
	v_mfma_f32_16x16x32_bf16 v[106:109], v[176:179], v[192:195], v[106:109]
	v_mfma_f32_16x16x32_bf16 v[98:101], v[168:171], v[200:203], v[98:101]
	v_mfma_f32_16x16x32_bf16 v[90:93], v[176:179], v[200:203], v[90:93]
	v_mfma_f32_16x16x32_bf16 v[82:85], v[168:171], v[212:215], v[82:85]
	v_mfma_f32_16x16x32_bf16 v[74:77], v[176:179], v[212:215], v[74:77]
	s_setprio 0
	s_barrier
	s_add_i32 s67, s59, s48
	v_lshl_add_u64 v[206:207], s[40:41], 0, v[132:133]
	s_mov_b32 m0, s67
	ds_read_b128 v[216:219], v155
	ds_read_b128 v[220:223], v155 offset:1024
	ds_read_b128 v[224:227], v155 offset:2048
	ds_read_b128 v[228:231], v155 offset:3072
	global_load_lds_dwordx4 v[206:207], off
	v_lshl_add_u64 v[232:233], s[40:41], 0, v[130:131]
	s_add_i32 m0, s67, 0x2000
	s_nop 0
	global_load_lds_dwordx4 v[232:233], off
	s_barrier
	s_waitcnt lgkmcnt(0)
	s_setprio 1
	s_waitcnt lgkmcnt(0)
	v_mfma_f32_16x16x32_bf16 v[118:121], v[216:219], v[180:183], v[118:121]
	v_mfma_f32_16x16x32_bf16 v[110:113], v[224:227], v[180:183], v[110:113]
	v_mfma_f32_16x16x32_bf16 v[102:105], v[216:219], v[188:191], v[102:105]
	v_mfma_f32_16x16x32_bf16 v[94:97], v[224:227], v[188:191], v[94:97]
	v_mfma_f32_16x16x32_bf16 v[86:89], v[216:219], v[196:199], v[86:89]
	v_mfma_f32_16x16x32_bf16 v[78:81], v[224:227], v[196:199], v[78:81]
	v_mfma_f32_16x16x32_bf16 v[70:73], v[216:219], v[208:211], v[70:73]
	v_mfma_f32_16x16x32_bf16 v[66:69], v[224:227], v[208:211], v[66:69]
	v_mfma_f32_16x16x32_bf16 v[118:121], v[220:223], v[184:187], v[118:121]
	v_mfma_f32_16x16x32_bf16 v[110:113], v[228:231], v[184:187], v[110:113]
	v_mfma_f32_16x16x32_bf16 v[102:105], v[220:223], v[192:195], v[102:105]
	v_mfma_f32_16x16x32_bf16 v[94:97], v[228:231], v[192:195], v[94:97]
	v_mfma_f32_16x16x32_bf16 v[86:89], v[220:223], v[200:203], v[86:89]
	v_mfma_f32_16x16x32_bf16 v[78:81], v[228:231], v[200:203], v[78:81]
	v_mfma_f32_16x16x32_bf16 v[70:73], v[220:223], v[212:215], v[70:73]
	v_mfma_f32_16x16x32_bf16 v[66:69], v[228:231], v[212:215], v[66:69]
	s_setprio 0
	s_mov_b32 m0, s49
	s_barrier
	ds_read_b128 v[180:183], v154 offset:16384
	ds_read_b128 v[184:187], v154 offset:17408
	ds_read_b128 v[188:191], v154 offset:18432
	ds_read_b128 v[192:195], v154 offset:19456
	ds_read_b128 v[196:199], v154 offset:20480
	ds_read_b128 v[200:203], v154 offset:21504
	ds_read_b128 v[208:211], v154 offset:22528
	ds_read_b128 v[212:215], v154 offset:23552
	global_load_lds_dwordx4 v134, s[44:45]
	s_mov_b32 m0, s50
	v_mov_b32_e32 v205, v135
	global_load_lds_dwordx4 v204, s[44:45]
	s_barrier
	s_waitcnt lgkmcnt(0)
	v_lshl_add_u64 v[234:235], s[44:45], 0, v[134:135]
	v_lshl_add_u64 v[204:205], s[44:45], 0, v[204:205]
	s_setprio 1
	s_waitcnt lgkmcnt(0)
	v_mfma_f32_16x16x32_bf16 v[62:65], v[164:167], v[180:183], v[62:65]
	v_mfma_f32_16x16x32_bf16 v[58:61], v[172:175], v[180:183], v[58:61]
	v_mfma_f32_16x16x32_bf16 v[46:49], v[164:167], v[188:191], v[46:49]
	v_mfma_f32_16x16x32_bf16 v[42:45], v[172:175], v[188:191], v[42:45]
	v_mfma_f32_16x16x32_bf16 v[30:33], v[164:167], v[196:199], v[30:33]
	v_mfma_f32_16x16x32_bf16 v[26:29], v[172:175], v[196:199], v[26:29]
	v_mfma_f32_16x16x32_bf16 v[14:17], v[164:167], v[208:211], v[14:17]
	v_mfma_f32_16x16x32_bf16 v[10:13], v[172:175], v[208:211], v[10:13]
	v_mfma_f32_16x16x32_bf16 v[62:65], v[168:171], v[184:187], v[62:65]
	v_mfma_f32_16x16x32_bf16 v[58:61], v[176:179], v[184:187], v[58:61]
	v_mfma_f32_16x16x32_bf16 v[46:49], v[168:171], v[192:195], v[46:49]
	v_mfma_f32_16x16x32_bf16 v[42:45], v[176:179], v[192:195], v[42:45]
	v_mfma_f32_16x16x32_bf16 v[30:33], v[168:171], v[200:203], v[30:33]
	v_mfma_f32_16x16x32_bf16 v[26:29], v[176:179], v[200:203], v[26:29]
	v_mfma_f32_16x16x32_bf16 v[14:17], v[168:171], v[212:215], v[14:17]
	v_mfma_f32_16x16x32_bf16 v[10:13], v[176:179], v[212:215], v[10:13]
	s_setprio 0
	s_barrier
	s_add_i32 s67, s60, s48
	v_lshl_add_u64 v[164:165], v[206:207], 0, s[4:5]
	s_mov_b32 m0, s67
	s_nop 0
	global_load_lds_dwordx4 v[164:165], off
	v_lshl_add_u64 v[164:165], v[232:233], 0, s[4:5]
	s_add_i32 m0, s67, 0x2000
	s_nop 0
	global_load_lds_dwordx4 v[164:165], off
	s_cmp_eq_u32 s82, 0
	s_cbranch_scc1 .Lpb9_p4n
	s_waitcnt vmcnt(14)
	v_cvt_pk_bf16_f32 v244, v244, v245
	v_cvt_pk_bf16_f32 v245, v246, v247
	v_cvt_pk_bf16_f32 v246, v248, v249
	v_cvt_pk_bf16_f32 v247, v250, v251
	global_store_dwordx4 v253, v[244:247], s[78:79] nt
	s_mov_b32 s82, 0
	s_waitcnt vmcnt(7)
	s_branch .Lpb9_p4j

; #define PG8_STAGE(bufoff, gbase, v0, v1) do { \
;         __builtin_amdgcn_global_load_lds((const unsigned*)((const char*)(gbase) + (v0)), (LAS unsigned*)(lds + (bufoff) + ldsw), 16, 0, 0); \
;         __builtin_amdgcn_global_load_lds((const unsigned*)((const char*)(gbase) + (v1)), (LAS unsigned*)(lds + (bufoff) + ldsw + 8192), 16, 0, 0); } while (0)
; #define PG8_LDA(dst, b, h) do { _Pragma("unroll") for (int m = 0; m < 4; ++m) _Pragma("unroll") for (int k = 0; k < 2; ++k) dst[m][k] = *(const LAS bf16x8*)(lds + PG8_SA(b, h) + aoff + m * 2048 + k * 1024); } while (0)
; #define PG8_LDB(dst, b, h) do { _Pragma("unroll") for (int n = 0; n < 2; ++n) _Pragma("unroll") for (int k = 0; k < 2; ++k) dst[n][k] = *(const LAS bf16x8*)(lds + PG8_SB(b, h) + boff + n * 2048 + k * 1024); } while (0)
; #define PG8_MMA(ai, bj, At, Bt) do { __builtin_amdgcn_s_setprio(1); _Pragma("unroll") for (int m = 0; m < 4; ++m) _Pragma("unroll") for (int n = 0; n < 2; ++n) _Pragma("unroll") for (int k = 0; k < 2; ++k) \
;         acc[ai][bj][m][n] = __builtin_amdgcn_mfma_f32_16x16x32_bf16(Bt[n][k], At[m][k], acc[ai][bj][m][n], 0, 0, 0); __builtin_amdgcn_s_setprio(0); } while (0)
; #define PG8_WAIT_V(n) asm volatile("s_waitcnt vmcnt(" #n ")" ::: "memory")
; #define PG8_BAR __builtin_amdgcn_s_barrier()
; #define PG8_SCHED __builtin_amdgcn_sched_barrier(0)
; template <class Epi, class Sched>
; __device__ __forceinline__ void gemm_phase(LAS unsigned char* lds, const int K, const Sched& S, const Epi& E) {
;     ...
;             PG8_WAIT_V(6); PG8_BAR; PG8_MMA(1, 1, At, B1); PG8_BAR;
;             PG8_LDB(B0, 1, 0); PG8_SCHED; PG8_LDA(At, 1, 0); PG8_STAGE(PG8_SA(0, 1), a2, x10, x11);
; __device__ __forceinline__ bool bg_decode(int st, int wg, int NW, int lane, KP kp, const float*& src, int& ldS, bf16_t*& dst, int& o2) {
;     ...
;         const int e = r >> 10, kc = (r >> 2) & 255, kind = (r >> 1) & 1, cc = r & 1, n = cc * 256 + lane;
;         ldS = FF; o2 = 256 * 8;
;         src = kp->in[27 + kind] + ((size_t)(l * NE + e) * D + kc * 8) * FF + n;
;         const int drow = (n >> 7) * 256 + kind * 128 + (n & 127);
;         dst = (bf16_t*)(ws + WS_WGU) + l * WGU_L + (size_t)e * 1024 * D + ((size_t)kc * 1024 + drow) * 8;
.Lpb9_p4j:
	s_barrier
	s_setprio 1
	v_mfma_f32_16x16x32_bf16 v[54:57], v[216:219], v[180:183], v[54:57]
	v_mfma_f32_16x16x32_bf16 v[50:53], v[224:227], v[180:183], v[50:53]
	v_mfma_f32_16x16x32_bf16 v[38:41], v[216:219], v[188:191], v[38:41]
	v_mfma_f32_16x16x32_bf16 v[34:37], v[224:227], v[188:191], v[34:37]
	v_mfma_f32_16x16x32_bf16 v[22:25], v[216:219], v[196:199], v[22:25]
	v_mfma_f32_16x16x32_bf16 v[18:21], v[224:227], v[196:199], v[18:21]
	v_mfma_f32_16x16x32_bf16 v[6:9], v[216:219], v[208:211], v[6:9]
	v_mfma_f32_16x16x32_bf16 v[2:5], v[224:227], v[208:211], v[2:5]
	v_mfma_f32_16x16x32_bf16 v[54:57], v[220:223], v[184:187], v[54:57]
	v_mfma_f32_16x16x32_bf16 v[50:53], v[228:231], v[184:187], v[50:53]
	v_mfma_f32_16x16x32_bf16 v[38:41], v[220:223], v[192:195], v[38:41]
	v_mfma_f32_16x16x32_bf16 v[34:37], v[228:231], v[192:195], v[34:37]
	v_mfma_f32_16x16x32_bf16 v[22:25], v[220:223], v[200:203], v[22:25]
	v_mfma_f32_16x16x32_bf16 v[18:21], v[228:231], v[200:203], v[18:21]
	v_mfma_f32_16x16x32_bf16 v[6:9], v[220:223], v[212:215], v[6:9]
	v_mfma_f32_16x16x32_bf16 v[2:5], v[228:231], v[212:215], v[2:5]
	s_setprio 0
	s_add_i32 s67, 0, 0x18000
	v_add_u32_e32 v134, s67, v151
	s_barrier
	ds_read_b128 v[164:167], v134
	ds_read_b128 v[168:171], v134 offset:1024
	ds_read_b128 v[172:175], v134 offset:2048
	ds_read_b128 v[176:179], v134 offset:3072
	s_mov_b32 m0, s51
	ds_read_b128 v[180:183], v154 offset:32768
	ds_read_b128 v[184:187], v154 offset:33792
	ds_read_b128 v[188:191], v154 offset:34816
	ds_read_b128 v[192:195], v154 offset:35840
	ds_read_b128 v[196:199], v154 offset:36864
	ds_read_b128 v[200:203], v154 offset:37888
	ds_read_b128 v[208:211], v154 offset:38912
	ds_read_b128 v[212:215], v154 offset:39936
	v_cndmask_b32_e32 v134, v140, v160, vcc
	global_load_lds_dwordx4 v139, s[44:45]
	s_mov_b32 m0, s52
	s_nop 0
	global_load_lds_dwordx4 v134, s[44:45]
	s_cmp_ge_u32 s70, 0x20000
	s_cbranch_scc1 .Lpb9_p5n
	s_cmp_eq_u32 s80, 0
	s_cbranch_scc0 .Lpb9_adv2
	s_cmp_ge_u32 s70, 0x18000
	s_cselect_b32 s84, 0x18000, 0
	s_cselect_b32 s83, 0x10000000, 0
	s_mov_b32 s81, 0x4030000
	s_cselect_b32 s81, 0x14430000, s81
	s_sub_u32 s84, s70, s84
	s_lshr_b32 s85, s84, 2
	s_lshl_b32 s85, s85, 14
	s_and_b32 s86, s84, 1
	s_lshl_b32 s87, s86, 10
	s_add_u32 s87, s87, s85
	s_add_u32 s87, s87, s83
	s_bitcmp1_b32 s84, 1
	s_cselect_b64 s[72:73], s[76:77], s[74:75]
	s_add_u32 s72, s72, s87
	s_addc_u32 s73, s73, 0
	s_add_u32 s88, s72, 0x2000
	s_addc_u32 s89, s73, 0
	s_lshl_b32 s86, s86, 13
	s_add_u32 s85, s85, s86
	s_and_b32 s86, s84, 2
	s_lshl_b32 s86, s86, 10
	s_add_u32 s85, s85, s86
	s_add_u32 s85, s85, s81
	v_add_u32_e32 v253, s85, v252
	s_movk_i32 s81, 0x400
	s_branch .Lpb9_ld2

; #define PG8_STAGE(bufoff, gbase, v0, v1) do { \
;         __builtin_amdgcn_global_load_lds((const unsigned*)((const char*)(gbase) + (v0)), (LAS unsigned*)(lds + (bufoff) + ldsw), 16, 0, 0); \
;         __builtin_amdgcn_global_load_lds((const unsigned*)((const char*)(gbase) + (v1)), (LAS unsigned*)(lds + (bufoff) + ldsw + 8192), 16, 0, 0); } while (0)
; #define PG8_LDA(dst, b, h) do { _Pragma("unroll") for (int m = 0; m < 4; ++m) _Pragma("unroll") for (int k = 0; k < 2; ++k) dst[m][k] = *(const LAS bf16x8*)(lds + PG8_SA(b, h) + aoff + m * 2048 + k * 1024); } while (0)
; #define PG8_LDB(dst, b, h) do { _Pragma("unroll") for (int n = 0; n < 2; ++n) _Pragma("unroll") for (int k = 0; k < 2; ++k) dst[n][k] = *(const LAS bf16x8*)(lds + PG8_SB(b, h) + boff + n * 2048 + k * 1024); } while (0)
; #define PG8_MMA(ai, bj, At, Bt) do { __builtin_amdgcn_s_setprio(1); _Pragma("unroll") for (int m = 0; m < 4; ++m) _Pragma("unroll") for (int n = 0; n < 2; ++n) _Pragma("unroll") for (int k = 0; k < 2; ++k) \
;         acc[ai][bj][m][n] = __builtin_amdgcn_mfma_f32_16x16x32_bf16(Bt[n][k], At[m][k], acc[ai][bj][m][n], 0, 0, 0); __builtin_amdgcn_s_setprio(0); } while (0)
; #define PG8_WAIT_V(n) asm volatile("s_waitcnt vmcnt(" #n ")" ::: "memory")
; #define PG8_WAIT_L(n) asm volatile("s_waitcnt lgkmcnt(" #n ")" ::: "memory")
; #define PG8_BAR __builtin_amdgcn_s_barrier()
; #define PG8_SCHED __builtin_amdgcn_sched_barrier(0)
; template <class Epi, class Sched>
; __device__ __forceinline__ void gemm_phase(LAS unsigned char* lds, const int K, const Sched& S, const Epi& E) {
;     ...
;             PG8_WAIT_L(8); PG8_BAR; PG8_WAIT_L(0); PG8_MMA(0, 0, At, B0); PG8_BAR; PG8_SCHED;
;             PG8_LDB(B1, 1, 1); PG8_STAGE(PG8_SB(1, 0), b3, voffB0, voffB1);
;             PG8_BAR; PG8_WAIT_L(0); PG8_MMA(0, 1, At, B1); PG8_BAR;
;             PG8_LDA(At, 1, 1); PG8_STAGE(PG8_SA(1, 0), a3, x00, x01);
;             PG8_BAR; PG8_WAIT_L(0); PG8_MMA(1, 0, At, B0); PG8_BAR; PG8_SCHED;
;             PG8_STAGE(PG8_SB(1, 1), b3 + hstep, voffB0, voffB1);
;             PG8_WAIT_V(6); PG8_BAR; PG8_MMA(1, 1, At, B1); PG8_BAR;
.Lpb9_p5n:
	s_waitcnt lgkmcnt(8)
	s_barrier
	s_waitcnt lgkmcnt(0)
	s_setprio 1
	s_waitcnt lgkmcnt(0)
	v_mfma_f32_16x16x32_bf16 v[126:129], v[164:167], v[180:183], v[126:129]
	v_mfma_f32_16x16x32_bf16 v[122:125], v[172:175], v[180:183], v[122:125]
	v_mfma_f32_16x16x32_bf16 v[114:117], v[164:167], v[188:191], v[114:117]
	v_mfma_f32_16x16x32_bf16 v[106:109], v[172:175], v[188:191], v[106:109]
	v_mfma_f32_16x16x32_bf16 v[98:101], v[164:167], v[196:199], v[98:101]
	v_mfma_f32_16x16x32_bf16 v[90:93], v[172:175], v[196:199], v[90:93]
	v_mfma_f32_16x16x32_bf16 v[82:85], v[164:167], v[208:211], v[82:85]
	v_mfma_f32_16x16x32_bf16 v[74:77], v[172:175], v[208:211], v[74:77]
	v_mfma_f32_16x16x32_bf16 v[126:129], v[168:171], v[184:187], v[126:129]
	v_mfma_f32_16x16x32_bf16 v[122:125], v[176:179], v[184:187], v[122:125]
	v_mfma_f32_16x16x32_bf16 v[114:117], v[168:171], v[192:195], v[114:117]
	v_mfma_f32_16x16x32_bf16 v[106:109], v[176:179], v[192:195], v[106:109]
	v_mfma_f32_16x16x32_bf16 v[98:101], v[168:171], v[200:203], v[98:101]
	v_mfma_f32_16x16x32_bf16 v[90:93], v[176:179], v[200:203], v[90:93]
	v_mfma_f32_16x16x32_bf16 v[82:85], v[168:171], v[212:215], v[82:85]
	v_mfma_f32_16x16x32_bf16 v[74:77], v[176:179], v[212:215], v[74:77]
	s_setprio 0
	s_barrier
	s_add_i32 s44, 0, 0x1c000
	s_add_i32 s45, s67, s48
	v_add_u32_e32 v134, s44, v151
	v_lshl_add_u64 v[206:207], s[42:43], 0, v[132:133]
	s_mov_b32 m0, s45
	ds_read_b128 v[216:219], v134
	ds_read_b128 v[220:223], v134 offset:1024
	ds_read_b128 v[224:227], v134 offset:2048
	ds_read_b128 v[228:231], v134 offset:3072
	global_load_lds_dwordx4 v[206:207], off
	v_lshl_add_u64 v[206:207], s[42:43], 0, v[130:131]
	s_add_i32 m0, s45, 0x2000
	s_nop 0
	global_load_lds_dwordx4 v[206:207], off
	s_barrier
	s_waitcnt lgkmcnt(0)
	s_setprio 1
	s_waitcnt lgkmcnt(0)
	v_mfma_f32_16x16x32_bf16 v[118:121], v[216:219], v[180:183], v[118:121]
	v_mfma_f32_16x16x32_bf16 v[110:113], v[224:227], v[180:183], v[110:113]
	v_mfma_f32_16x16x32_bf16 v[102:105], v[216:219], v[188:191], v[102:105]
	v_mfma_f32_16x16x32_bf16 v[94:97], v[224:227], v[188:191], v[94:97]
	v_mfma_f32_16x16x32_bf16 v[86:89], v[216:219], v[196:199], v[86:89]
	v_mfma_f32_16x16x32_bf16 v[78:81], v[224:227], v[196:199], v[78:81]
	v_mfma_f32_16x16x32_bf16 v[70:73], v[216:219], v[208:211], v[70:73]
	v_mfma_f32_16x16x32_bf16 v[66:69], v[224:227], v[208:211], v[66:69]
	v_mfma_f32_16x16x32_bf16 v[118:121], v[220:223], v[184:187], v[118:121]
	v_mfma_f32_16x16x32_bf16 v[110:113], v[228:231], v[184:187], v[110:113]
	v_mfma_f32_16x16x32_bf16 v[102:105], v[220:223], v[192:195], v[102:105]
	v_mfma_f32_16x16x32_bf16 v[94:97], v[228:231], v[192:195], v[94:97]
	v_mfma_f32_16x16x32_bf16 v[86:89], v[220:223], v[200:203], v[86:89]
	v_mfma_f32_16x16x32_bf16 v[78:81], v[228:231], v[200:203], v[78:81]
	v_mfma_f32_16x16x32_bf16 v[70:73], v[220:223], v[212:215], v[70:73]
	v_mfma_f32_16x16x32_bf16 v[66:69], v[228:231], v[212:215], v[66:69]
	s_setprio 0
	s_mov_b32 m0, s55
	v_lshl_add_u64 v[206:207], v[234:235], 0, s[12:13]
	s_barrier
	ds_read_b128 v[180:183], v154 offset:49152
	ds_read_b128 v[184:187], v154 offset:50176
	ds_read_b128 v[188:191], v154 offset:51200
	ds_read_b128 v[192:195], v154 offset:52224
	ds_read_b128 v[196:199], v154 offset:53248
	ds_read_b128 v[200:203], v154 offset:54272
	ds_read_b128 v[208:211], v154 offset:55296
	ds_read_b128 v[212:215], v154 offset:56320
	global_load_lds_dwordx4 v[206:207], off
	v_lshl_add_u64 v[204:205], v[204:205], 0, s[12:13]
	s_mov_b32 m0, s56
	s_nop 0
	global_load_lds_dwordx4 v[204:205], off
	s_barrier
	s_waitcnt lgkmcnt(0)
	s_setprio 1
	s_waitcnt lgkmcnt(0)
	v_mfma_f32_16x16x32_bf16 v[62:65], v[164:167], v[180:183], v[62:65]
	v_mfma_f32_16x16x32_bf16 v[58:61], v[172:175], v[180:183], v[58:61]
	v_mfma_f32_16x16x32_bf16 v[46:49], v[164:167], v[188:191], v[46:49]
	v_mfma_f32_16x16x32_bf16 v[42:45], v[172:175], v[188:191], v[42:45]
	v_mfma_f32_16x16x32_bf16 v[30:33], v[164:167], v[196:199], v[30:33]
	v_mfma_f32_16x16x32_bf16 v[26:29], v[172:175], v[196:199], v[26:29]
	v_mfma_f32_16x16x32_bf16 v[14:17], v[164:167], v[208:211], v[14:17]
	v_mfma_f32_16x16x32_bf16 v[10:13], v[172:175], v[208:211], v[10:13]
	v_mfma_f32_16x16x32_bf16 v[62:65], v[168:171], v[184:187], v[62:65]
	v_mfma_f32_16x16x32_bf16 v[58:61], v[176:179], v[184:187], v[58:61]
	v_mfma_f32_16x16x32_bf16 v[46:49], v[168:171], v[192:195], v[46:49]
	v_mfma_f32_16x16x32_bf16 v[42:45], v[176:179], v[192:195], v[42:45]
	v_mfma_f32_16x16x32_bf16 v[30:33], v[168:171], v[200:203], v[30:33]
	v_mfma_f32_16x16x32_bf16 v[26:29], v[176:179], v[200:203], v[26:29]
	v_mfma_f32_16x16x32_bf16 v[14:17], v[168:171], v[212:215], v[14:17]
	v_mfma_f32_16x16x32_bf16 v[10:13], v[176:179], v[212:215], v[10:13]
	s_setprio 0
	s_barrier
	s_add_u32 s40, s40, 0x40800
	s_addc_u32 s41, s41, 0
	s_add_i32 s42, s44, s48
	v_lshl_add_u64 v[164:165], s[40:41], 0, v[132:133]
	s_mov_b32 m0, s42
	s_nop 0
	global_load_lds_dwordx4 v[164:165], off
	v_lshl_add_u64 v[164:165], s[40:41], 0, v[130:131]
	s_add_i32 m0, s42, 0x2000
	s_nop 0
	global_load_lds_dwordx4 v[164:165], off
	s_cmp_eq_u32 s82, 0
	s_cbranch_scc1 .Lpb9_p8n
	s_waitcnt vmcnt(14)
	s_branch .Lpb9_p8j

; #define PG8_MMA(ai, bj, At, Bt) do { __builtin_amdgcn_s_setprio(1); _Pragma("unroll") for (int m = 0; m < 4; ++m) _Pragma("unroll") for (int n = 0; n < 2; ++n) _Pragma("unroll") for (int k = 0; k < 2; ++k) \
;         acc[ai][bj][m][n] = __builtin_amdgcn_mfma_f32_16x16x32_bf16(Bt[n][k], At[m][k], acc[ai][bj][m][n], 0, 0, 0); __builtin_amdgcn_s_setprio(0); } while (0)
; #define PG8_WAIT_V(n) asm volatile("s_waitcnt vmcnt(" #n ")" ::: "memory")
; #define PG8_BAR __builtin_amdgcn_s_barrier()
; __device__ __forceinline__ unsigned pk4_fp8(float a, float b, float c, float d) { int w = 0; w = __builtin_amdgcn_cvt_pk_fp8_f32(a, b, w, false); w = __builtin_amdgcn_cvt_pk_fp8_f32(c, d, w, true); return (unsigned)w; }
; template <class Epi, class Sched>
; __device__ __forceinline__ void gemm_phase(LAS unsigned char* lds, const int K, const Sched& S, const Epi& E) {
;     ...
;             PG8_WAIT_V(6); PG8_BAR; PG8_MMA(1, 1, At, B1); PG8_BAR;
;         }
;         E(acc, cur, wr, wc, fr, fq);
;     __device__ __forceinline__ void operator()(const f32x4 (&acc)[2][2][4][2], const Unit& u, int wr, int wc, int fr, int fq) const {
;         const int row0 = u.rbase + wr * 64 + fr, col0 = u.pn * BM + wc * 32 + 8 * fq;
; #pragma unroll
;         for (int ai = 0; ai < 2; ++ai)
; #pragma unroll
;             for (int m = 0; m < 4; ++m) { unsigned char* rowp = O + (size_t)(row0 + ai * HALF + m * 16) * ldc + col0;
; #pragma unroll
;                 for (int bj = 0; bj < 2; ++bj) { const f32x4 v0 = acc[ai][bj][m][0] * scale, v1 = acc[ai][bj][m][1] * scale;
;                     u32x2 w; w.x = pk4_fp8(v0[0], v0[1], v0[2], v0[3]); w.y = pk4_fp8(v1[0], v1[1], v1[2], v1[3]);
.Lpb9_p8j:
	s_barrier
	s_setprio 1
	v_mfma_f32_16x16x32_bf16 v[54:57], v[216:219], v[180:183], v[54:57]
	v_mfma_f32_16x16x32_bf16 v[50:53], v[224:227], v[180:183], v[50:53]
	v_mfma_f32_16x16x32_bf16 v[38:41], v[216:219], v[188:191], v[38:41]
	v_mfma_f32_16x16x32_bf16 v[34:37], v[224:227], v[188:191], v[34:37]
	v_mfma_f32_16x16x32_bf16 v[22:25], v[216:219], v[196:199], v[22:25]
	v_mfma_f32_16x16x32_bf16 v[18:21], v[224:227], v[196:199], v[18:21]
	v_mfma_f32_16x16x32_bf16 v[6:9], v[216:219], v[208:211], v[6:9]
	v_mfma_f32_16x16x32_bf16 v[2:5], v[224:227], v[208:211], v[2:5]
	v_mfma_f32_16x16x32_bf16 v[54:57], v[220:223], v[184:187], v[54:57]
	v_mfma_f32_16x16x32_bf16 v[50:53], v[228:231], v[184:187], v[50:53]
	v_mfma_f32_16x16x32_bf16 v[38:41], v[220:223], v[192:195], v[38:41]
	v_mfma_f32_16x16x32_bf16 v[34:37], v[228:231], v[192:195], v[34:37]
	v_mfma_f32_16x16x32_bf16 v[22:25], v[220:223], v[200:203], v[22:25]
	v_mfma_f32_16x16x32_bf16 v[18:21], v[228:231], v[200:203], v[18:21]
	v_mfma_f32_16x16x32_bf16 v[6:9], v[220:223], v[212:215], v[6:9]
	v_mfma_f32_16x16x32_bf16 v[2:5], v[228:231], v[212:215], v[2:5]
	s_setprio 0
	s_add_i32 s66, s66, 2
	s_add_u32 s29, s29, 0x80000
	s_addc_u32 s31, s31, 0
	s_add_u32 s38, s38, 0x100
	s_addc_u32 s39, s39, 0
	s_cmp_gt_u32 s66, 5
	s_barrier
	s_cbranch_scc0 .LBB0_1161
	v_pk_mul_f32 v[126:127], v[126:127], s[14:15] op_sel_hi:[1,0]
	v_mov_b32_e32 v142, v135
	v_cvt_pk_fp8_f32 v142, v126, v127
	v_pk_mul_f32 v[122:123], v[122:123], s[14:15] op_sel_hi:[1,0]
	v_mov_b32_e32 v143, v135
	v_cvt_pk_fp8_f32 v143, v122, v123
	v_pk_mul_f32 v[122:123], v[128:129], s[14:15] op_sel_hi:[1,0]
	v_pk_mul_f32 v[118:119], v[118:119], s[14:15] op_sel_hi:[1,0]
	v_cvt_pk_fp8_f32 v142, v122, v123 op_sel:[0,0,1]
	v_mov_b32_e32 v122, v135
	v_cvt_pk_fp8_f32 v122, v118, v119
	v_pk_mul_f32 v[114:115], v[114:115], s[14:15] op_sel_hi:[1,0]
	v_mov_b32_e32 v118, v135
	v_cvt_pk_fp8_f32 v118, v114, v115
	v_pk_mul_f32 v[106:107], v[106:107], s[14:15] op_sel_hi:[1,0]
	v_mov_b32_e32 v119, v135
	v_cvt_pk_fp8_f32 v119, v106, v107
	v_pk_mul_f32 v[106:107], v[116:117], s[14:15] op_sel_hi:[1,0]
	v_pk_mul_f32 v[94:95], v[94:95], s[14:15] op_sel_hi:[1,0]
	v_cvt_pk_fp8_f32 v118, v106, v107 op_sel:[0,0,1]
	v_mov_b32_e32 v107, v135
	v_cvt_pk_fp8_f32 v107, v94, v95
	v_pk_mul_f32 v[96:97], v[96:97], s[14:15] op_sel_hi:[1,0]
	v_pk_mul_f32 v[90:91], v[90:91], s[14:15] op_sel_hi:[1,0]
	v_pk_mul_f32 v[78:79], v[78:79], s[14:15] op_sel_hi:[1,0]
	v_cvt_pk_fp8_f32 v107, v96, v97 op_sel:[0,0,1]
	v_pk_mul_f32 v[96:97], v[98:99], s[14:15] op_sel_hi:[1,0]
	v_mov_b32_e32 v98, v135
	v_cvt_pk_fp8_f32 v98, v96, v97
	v_mov_b32_e32 v99, v135
	v_cvt_pk_fp8_f32 v99, v90, v91
	v_pk_mul_f32 v[90:91], v[100:101], s[14:15] op_sel_hi:[1,0]
	v_pk_mul_f32 v[80:81], v[80:81], s[14:15] op_sel_hi:[1,0]
	v_cvt_pk_fp8_f32 v98, v90, v91 op_sel:[0,0,1]
	v_mov_b32_e32 v91, v135
	v_cvt_pk_fp8_f32 v91, v78, v79
	v_pk_mul_f32 v[74:75], v[74:75], s[14:15] op_sel_hi:[1,0]
	v_pk_mul_f32 v[66:67], v[66:67], s[14:15] op_sel_hi:[1,0]
	v_pk_mul_f32 v[68:69], v[68:69], s[14:15] op_sel_hi:[1,0]
	v_cvt_pk_fp8_f32 v91, v80, v81 op_sel:[0,0,1]
	v_pk_mul_f32 v[80:81], v[82:83], s[14:15] op_sel_hi:[1,0]
	v_mov_b32_e32 v82, v135
	v_cvt_pk_fp8_f32 v82, v80, v81
	v_mov_b32_e32 v83, v135
	v_cvt_pk_fp8_f32 v83, v74, v75
	v_pk_mul_f32 v[74:75], v[84:85], s[14:15] op_sel_hi:[1,0]
	v_pk_mul_f32 v[62:63], v[62:63], s[14:15] op_sel_hi:[1,0]
	v_cvt_pk_fp8_f32 v82, v74, v75 op_sel:[0,0,1]
	v_mov_b32_e32 v75, v135
	v_cvt_pk_fp8_f32 v75, v66, v67
	v_pk_mul_f32 v[58:59], v[58:59], s[14:15] op_sel_hi:[1,0]
	v_pk_mul_f32 v[50:51], v[50:51], s[14:15] op_sel_hi:[1,0]
	v_pk_mul_f32 v[52:53], v[52:53], s[14:15] op_sel_hi:[1,0]
	v_cvt_pk_fp8_f32 v75, v68, v69 op_sel:[0,0,1]
	v_mov_b32_e32 v68, v135
	v_cvt_pk_fp8_f32 v68, v62, v63
	v_mov_b32_e32 v69, v135
	v_cvt_pk_fp8_f32 v69, v58, v59
	v_pk_mul_f32 v[58:59], v[64:65], s[14:15] op_sel_hi:[1,0]
	v_pk_mul_f32 v[46:47], v[46:47], s[14:15] op_sel_hi:[1,0]
	v_cvt_pk_fp8_f32 v68, v58, v59 op_sel:[0,0,1]
	v_mov_b32_e32 v59, v135
	v_cvt_pk_fp8_f32 v59, v50, v51
	v_pk_mul_f32 v[42:43], v[42:43], s[14:15] op_sel_hi:[1,0]
	v_pk_mul_f32 v[34:35], v[34:35], s[14:15] op_sel_hi:[1,0]
	v_pk_mul_f32 v[36:37], v[36:37], s[14:15] op_sel_hi:[1,0]
	v_cvt_pk_fp8_f32 v59, v52, v53 op_sel:[0,0,1]
	v_mov_b32_e32 v52, v135
	v_cvt_pk_fp8_f32 v52, v46, v47
	v_mov_b32_e32 v53, v135
	v_cvt_pk_fp8_f32 v53, v42, v43
	v_pk_mul_f32 v[42:43], v[48:49], s[14:15] op_sel_hi:[1,0]
	v_pk_mul_f32 v[30:31], v[30:31], s[14:15] op_sel_hi:[1,0]
	v_cvt_pk_fp8_f32 v52, v42, v43 op_sel:[0,0,1]
	v_mov_b32_e32 v43, v135
	v_cvt_pk_fp8_f32 v43, v34, v35
	v_add_u32_e32 v138, v161, v137
	v_pk_mul_f32 v[102:103], v[102:103], s[14:15] op_sel_hi:[1,0]
	v_mov_b32_e32 v106, v135
	v_cvt_pk_fp8_f32 v43, v36, v37 op_sel:[0,0,1]
	v_mov_b32_e32 v36, v135
	v_cvt_pk_fp8_f32 v36, v30, v31
	v_pk_mul_f32 v[26:27], v[26:27], s[14:15] op_sel_hi:[1,0]
	v_mov_b32_e32 v37, v135
	v_ashrrev_i32_e32 v139, 31, v138
	v_pk_mul_f32 v[110:111], v[110:111], s[14:15] op_sel_hi:[1,0]
	v_mov_b32_e32 v123, v135
	v_cvt_pk_fp8_f32 v106, v102, v103
	v_cvt_pk_fp8_f32 v37, v26, v27
	v_pk_mul_f32 v[26:27], v[32:33], s[14:15] op_sel_hi:[1,0]
	v_lshl_or_b32 v140, s65, 8, v152
	v_lshlrev_b64 v[138:139], 11, v[138:139]
	v_cvt_pk_fp8_f32 v123, v110, v111
	v_pk_mul_f32 v[110:111], v[120:121], s[14:15] op_sel_hi:[1,0]
	v_pk_mul_f32 v[86:87], v[86:87], s[14:15] op_sel_hi:[1,0]
; #define PG8_WAIT_V(n) asm volatile("s_waitcnt vmcnt(" #n ")" ::: "memory")
; #define PG8_BAR __builtin_amdgcn_s_barrier()
; __device__ __forceinline__ unsigned pk4_fp8(float a, float b, float c, float d) { int w = 0; w = __builtin_amdgcn_cvt_pk_fp8_f32(a, b, w, false); w = __builtin_amdgcn_cvt_pk_fp8_f32(c, d, w, true); return (unsigned)w; }
; template <class Epi, class Sched>
; __device__ __forceinline__ void gemm_phase(LAS unsigned char* lds, const int K, const Sched& S, const Epi& E) {
;     ...
;         if (!has_next) break;
; #pragma unroll
;         for (int a = 0; a < 2; ++a)
; #pragma unroll
;             for (int b = 0; b < 2; ++b)
; #pragma unroll
;                 for (int m = 0; m < 4; ++m)
; #pragma unroll
;                     for (int n = 0; n < 2; ++n) acc[a][b][m][n] = (f32x4){0.f, 0.f, 0.f, 0.f};
;         cur = nxt; cB = nB; c00 = n00; c01 = n01; c10 = n10; c11 = n11; ++ui;
;     }
;     PG8_WAIT_V(0);
;     if (wr == 0) PG8_BAR;
;     PG8_BAR;
;     __device__ __forceinline__ void operator()(const f32x4 (&acc)[2][2][4][2], const Unit& u, int wr, int wc, int fr, int fq) const {
;     ...
; #pragma unroll
;         for (int ai = 0; ai < 2; ++ai)
; #pragma unroll
;             for (int m = 0; m < 4; ++m) { unsigned char* rowp = O + (size_t)(row0 + ai * HALF + m * 16) * ldc + col0;
; #pragma unroll
;                 for (int bj = 0; bj < 2; ++bj) { const f32x4 v0 = acc[ai][bj][m][0] * scale, v1 = acc[ai][bj][m][1] * scale;
;                     u32x2 w; w.x = pk4_fp8(v0[0], v0[1], v0[2], v0[3]); w.y = pk4_fp8(v1[0], v1[1], v1[2], v1[3]);
;                     *(u32x2*)(rowp + bj * HALF) = w; } }
	v_mov_b32_e32 v90, v135
	v_cvt_pk_fp8_f32 v36, v26, v27 op_sel:[0,0,1]
	v_pk_mul_f32 v[18:19], v[18:19], s[14:15] op_sel_hi:[1,0]
	v_mov_b32_e32 v27, v135
	v_ashrrev_i32_e32 v141, 31, v140
	v_cvt_pk_fp8_f32 v122, v110, v111 op_sel:[0,0,1]
	v_lshl_add_u64 v[110:111], s[6:7], 0, v[138:139]
	v_cvt_pk_fp8_f32 v90, v86, v87
	v_cvt_pk_fp8_f32 v27, v18, v19
	v_lshl_add_u64 v[110:111], v[110:111], 0, v[140:141]
	v_pk_mul_f32 v[94:95], v[104:105], s[14:15] op_sel_hi:[1,0]
	v_pk_mul_f32 v[70:71], v[70:71], s[14:15] op_sel_hi:[1,0]
	v_mov_b32_e32 v74, v135
	v_cvt_pk_fp8_f32 v106, v94, v95 op_sel:[0,0,1]
	v_add_co_u32_e32 v94, vcc, s58, v110
	v_cvt_pk_fp8_f32 v74, v70, v71
	s_nop 0
	v_addc_co_u32_e32 v95, vcc, 0, v111, vcc
	v_pk_mul_f32 v[78:79], v[88:89], s[14:15] op_sel_hi:[1,0]
	v_pk_mul_f32 v[54:55], v[54:55], s[14:15] op_sel_hi:[1,0]
	v_mov_b32_e32 v58, v135
	v_pk_mul_f32 v[20:21], v[20:21], s[14:15] op_sel_hi:[1,0]
	v_cvt_pk_fp8_f32 v90, v78, v79 op_sel:[0,0,1]
	v_add_co_u32_e32 v78, vcc, s54, v110
	v_cvt_pk_fp8_f32 v58, v54, v55
	v_cvt_pk_fp8_f32 v27, v20, v21 op_sel:[0,0,1]
	v_pk_mul_f32 v[14:15], v[14:15], s[14:15] op_sel_hi:[1,0]
	v_mov_b32_e32 v20, v135
	v_addc_co_u32_e32 v79, vcc, 0, v111, vcc
	v_pk_mul_f32 v[66:67], v[72:73], s[14:15] op_sel_hi:[1,0]
	v_pk_mul_f32 v[38:39], v[38:39], s[14:15] op_sel_hi:[1,0]
	v_mov_b32_e32 v42, v135
	v_cvt_pk_fp8_f32 v20, v14, v15
	v_cvt_pk_fp8_f32 v74, v66, v67 op_sel:[0,0,1]
	v_add_co_u32_e32 v66, vcc, s57, v110
	v_cvt_pk_fp8_f32 v42, v38, v39
	s_nop 0
	v_addc_co_u32_e32 v67, vcc, 0, v111, vcc
	v_pk_mul_f32 v[50:51], v[56:57], s[14:15] op_sel_hi:[1,0]
	v_pk_mul_f32 v[22:23], v[22:23], s[14:15] op_sel_hi:[1,0]
	v_mov_b32_e32 v26, v135
	v_pk_mul_f32 v[10:11], v[10:11], s[14:15] op_sel_hi:[1,0]
	v_mov_b32_e32 v21, v135
	v_cvt_pk_fp8_f32 v58, v50, v51 op_sel:[0,0,1]
	v_add_co_u32_e32 v50, vcc, s61, v110
	v_cvt_pk_fp8_f32 v26, v22, v23
	v_cvt_pk_fp8_f32 v21, v10, v11
	v_pk_mul_f32 v[10:11], v[16:17], s[14:15] op_sel_hi:[1,0]
	v_addc_co_u32_e32 v51, vcc, 0, v111, vcc
	v_pk_mul_f32 v[34:35], v[40:41], s[14:15] op_sel_hi:[1,0]
	v_cvt_pk_fp8_f32 v20, v10, v11 op_sel:[0,0,1]
	v_pk_mul_f32 v[6:7], v[6:7], s[14:15] op_sel_hi:[1,0]
	v_pk_mul_f32 v[2:3], v[2:3], s[14:15] op_sel_hi:[1,0]
	v_mov_b32_e32 v10, v135
	v_mov_b32_e32 v11, v135
	v_cvt_pk_fp8_f32 v42, v34, v35 op_sel:[0,0,1]
	v_add_co_u32_e32 v34, vcc, s62, v110
	v_cvt_pk_fp8_f32 v10, v6, v7
	v_cvt_pk_fp8_f32 v11, v2, v3
	v_addc_co_u32_e32 v35, vcc, 0, v111, vcc
	v_pk_mul_f32 v[18:19], v[24:25], s[14:15] op_sel_hi:[1,0]
	v_pk_mul_f32 v[124:125], v[124:125], s[14:15] op_sel_hi:[1,0]
	v_pk_mul_f32 v[108:109], v[108:109], s[14:15] op_sel_hi:[1,0]
	v_pk_mul_f32 v[92:93], v[92:93], s[14:15] op_sel_hi:[1,0]
	v_pk_mul_f32 v[76:77], v[76:77], s[14:15] op_sel_hi:[1,0]
	v_pk_mul_f32 v[60:61], v[60:61], s[14:15] op_sel_hi:[1,0]
	v_pk_mul_f32 v[44:45], v[44:45], s[14:15] op_sel_hi:[1,0]
	v_pk_mul_f32 v[28:29], v[28:29], s[14:15] op_sel_hi:[1,0]
	v_cvt_pk_fp8_f32 v26, v18, v19 op_sel:[0,0,1]
	v_add_co_u32_e32 v18, vcc, s63, v110
	v_pk_mul_f32 v[12:13], v[12:13], s[14:15] op_sel_hi:[1,0]
	v_cvt_pk_fp8_f32 v143, v124, v125 op_sel:[0,0,1]
	v_pk_mul_f32 v[112:113], v[112:113], s[14:15] op_sel_hi:[1,0]
	v_cvt_pk_fp8_f32 v119, v108, v109 op_sel:[0,0,1]
	v_cvt_pk_fp8_f32 v99, v92, v93 op_sel:[0,0,1]
	v_cvt_pk_fp8_f32 v83, v76, v77 op_sel:[0,0,1]
	v_cvt_pk_fp8_f32 v69, v60, v61 op_sel:[0,0,1]
	v_cvt_pk_fp8_f32 v53, v44, v45 op_sel:[0,0,1]
	v_cvt_pk_fp8_f32 v37, v28, v29 op_sel:[0,0,1]
	v_addc_co_u32_e32 v19, vcc, 0, v111, vcc
	v_cvt_pk_fp8_f32 v21, v12, v13 op_sel:[0,0,1]
	v_pk_mul_f32 v[2:3], v[8:9], s[14:15] op_sel_hi:[1,0]
	v_pk_mul_f32 v[4:5], v[4:5], s[14:15] op_sel_hi:[1,0]
	v_cvt_pk_fp8_f32 v123, v112, v113 op_sel:[0,0,1]
	v_cvt_pk_fp8_f32 v10, v2, v3 op_sel:[0,0,1]
	v_cvt_pk_fp8_f32 v11, v4, v5 op_sel:[0,0,1]
	v_add_co_u32_e32 v2, vcc, s64, v110
	v_mov_b32_e32 v161, v156
	s_nop 0
	v_addc_co_u32_e32 v3, vcc, 0, v111, vcc
	s_and_b64 vcc, exec, s[34:35]
	s_mov_b32 s65, s28
	v_mov_b32_e32 v162, v157
	v_mov_b32_e32 v136, v158
	v_mov_b32_e32 v138, v159
	v_mov_b32_e32 v140, v160
	s_mov_b64 s[38:39], s[36:37]
	global_store_dwordx2 v[110:111], v[142:143], off
	global_store_dwordx2 v[110:111], v[122:123], off offset:128
	v_lshl_add_u64 v[112:113], v[110:111], 0, s[16:17]
	global_store_dwordx2 v[94:95], v[118:119], off
	global_store_dwordx2 v[112:113], v[106:107], off offset:128
	v_lshl_add_u64 v[94:95], v[110:111], 0, s[18:19]
	global_store_dwordx2 v[78:79], v[98:99], off
	global_store_dwordx2 v[94:95], v[90:91], off offset:128
	v_lshl_add_u64 v[78:79], v[110:111], 0, s[20:21]
	global_store_dwordx2 v[66:67], v[82:83], off
	global_store_dwordx2 v[78:79], v[74:75], off offset:128
	v_lshl_add_u64 v[66:67], v[110:111], 0, s[10:11]
	global_store_dwordx2 v[50:51], v[68:69], off
	global_store_dwordx2 v[66:67], v[58:59], off offset:128
	v_lshl_add_u64 v[50:51], v[110:111], 0, s[22:23]
	global_store_dwordx2 v[34:35], v[52:53], off
	global_store_dwordx2 v[50:51], v[42:43], off offset:128
	v_lshl_add_u64 v[34:35], v[110:111], 0, s[24:25]
	global_store_dwordx2 v[18:19], v[36:37], off
	global_store_dwordx2 v[34:35], v[26:27], off offset:128
	v_lshl_add_u64 v[18:19], v[110:111], 0, s[26:27]
	global_store_dwordx2 v[2:3], v[20:21], off
	global_store_dwordx2 v[18:19], v[10:11], off offset:128
	s_cbranch_vccz .LBB0_1156
	s_waitcnt vmcnt(0)
	s_cmpk_gt_u32 s33, 0xff
	s_cbranch_scc1 .LBB0_1165
	s_barrier

; __device__ __forceinline__ bool bg_decode(int st, int wg, int NW, int lane, KP kp, const float*& src, int& ldS, bf16_t*& dst, int& o2) {
;     ...
;     if (r < 65536) {
;         const int e = r >> 10, kc = (r >> 2) & 255, kind = (r >> 1) & 1, cc = r & 1, n = cc * 256 + lane;
;         ldS = FF; o2 = 256 * 8;
;         src = kp->in[27 + kind] + ((size_t)(l * NE + e) * D + kc * 8) * FF + n;
;         const int drow = (n >> 7) * 256 + kind * 128 + (n & 127);
;         dst = (bf16_t*)(ws + WS_WGU) + l * WGU_L + (size_t)e * 1024 * D + ((size_t)kc * 1024 + drow) * 8;
.Lpb9_d1:
	s_cmp_ge_u32 s70, 0x20000
	s_cbranch_scc1 .Lpb9_dend
	s_cmp_eq_u32 s80, 0
	s_cbranch_scc0 .Lpb9_adv1
	s_cmp_ge_u32 s70, 0x18000
	s_cselect_b32 s84, 0x18000, 0
	s_cselect_b32 s83, 0x10000000, 0
	s_mov_b32 s81, 0x4030000
	s_cselect_b32 s81, 0x14430000, s81
	s_sub_u32 s84, s70, s84
	s_lshr_b32 s85, s84, 2
	s_lshl_b32 s85, s85, 14
	s_and_b32 s86, s84, 1
	s_lshl_b32 s87, s86, 10
	s_add_u32 s87, s87, s85
	s_add_u32 s87, s87, s83
	s_bitcmp1_b32 s84, 1
	s_cselect_b64 s[72:73], s[76:77], s[74:75]
	s_add_u32 s72, s72, s87
	s_addc_u32 s73, s73, 0
	s_add_u32 s88, s72, 0x2000
	s_addc_u32 s89, s73, 0
	s_lshl_b32 s86, s86, 13
	s_add_u32 s85, s85, s86
	s_and_b32 s86, s84, 2
	s_lshl_b32 s86, s86, 10
	s_add_u32 s85, s85, s86
	s_add_u32 s85, s85, s81
	v_add_u32_e32 v253, s85, v252
	s_movk_i32 s81, 0x400
	s_branch .Lpb9_ld1
